# K-loop: s_setprio 0 moved behind the barrier that closes each MFMA segment (one instruction less on the MFMA segment's tail), on top of one raise per segment
# speedup vs baseline: 1.0081x; 1.0081x over previous
; #define PG8_STAGE(bufoff, gbase, voff) do { _Pragma("unroll") for (int _i = 0; _i < 2; ++_i) \
;         __builtin_amdgcn_global_load_lds((const unsigned*)((const char*)(gbase) + (voff)[_i]), (PG8_LAS unsigned*)(lds + (bufoff) + ldsw + _i * 8192), 16, 0, 0); } while (0)
; #define PG8_LDA(dst, b, h) do { _Pragma("unroll") for (int m = 0; m < 4; ++m) { const bf16x8 f0_ = *(const PG8_LAS bf16x8*)(lds + PG8_SA(b, h) + aoff + m * 2048), f1_ = *(const PG8_LAS bf16x8*)(lds + PG8_SA(b, h) + aoff + m * 2048 + 1024); dst[m].set(f0_, f1_); } } while (0)
; #define PG8_LDB(dst, b, h) do { _Pragma("unroll") for (int n = 0; n < 2; ++n) { const bf16x8 f0_ = *(const PG8_LAS bf16x8*)(lds + PG8_SB(b, h) + boff + n * 2048), f1_ = *(const PG8_LAS bf16x8*)(lds + PG8_SB(b, h) + boff + n * 2048 + 1024); dst[n].set(f0_, f1_); } } while (0)
; #define PG8_WAIT_V(n) asm volatile("s_waitcnt vmcnt(" #n ")" ::: "memory")
; #define PG8_WAIT_L(n) asm volatile("s_waitcnt lgkmcnt(" #n ")" ::: "memory")
; #define PG8_BAR __builtin_amdgcn_s_barrier()
; #define PG8_SCHED __builtin_amdgcn_sched_barrier(0)
; template <class Epi, class Sched, bool ALIGN_EPI = false, bool SP2 = false>
; __device__ __forceinline__ void gemm_phase(PG8_LAS unsigned char* lds, const Gemm g, const Sched& S, const Epi& E) {
;     ...
;             PG8_LDB(B0, 0, 0); PG8_LDB(B1, 0, 1); PG8_SCHED; PG8_LDA(At, 0, 0); PG8_STAGE(PG8_SA(1, 1), a1 + hstep, voffA);
;             PG8_WAIT_V(8); PG8_WAIT_L(0); PG8_BAR; PG8_MMA(0, 0, At, B0); PG8_MMA(0, 1, At, B1); PG8_BAR; PG8_SCHED;
;             PG8_LDA(At, 0, 1); PG8_STAGE(PG8_SB(0, 0), b2, voffB); PG8_STAGE(PG8_SB(0, 1), b2 + hstepB, voffB); PG8_STAGE(PG8_SA(0, 0), a2, voffA);
;             PG8_WAIT_V(8); PG8_WAIT_L(0); PG8_BAR; PG8_MMA(1, 0, At, B0); PG8_MMA(1, 1, At, B1); PG8_BAR; PG8_SCHED;
.Lkr0_a:
	v_lshl_add_u64 v[190:191], s[2:3], 0, v[174:175]
	s_add_i32 m0, s58, 0xc000
	ds_read_b128 v[182:185], v205
	ds_read_b128 v[186:189], v205 offset:1024
	ds_read_b128 v[212:215], v205 offset:2048
	ds_read_b128 v[216:219], v205 offset:3072
	ds_read_b128 v[220:223], v205 offset:4096
	ds_read_b128 v[224:227], v205 offset:5120
	ds_read_b128 v[228:231], v205 offset:6144
	ds_read_b128 v[232:235], v205 offset:7168
	global_load_lds_dwordx4 v[190:191], off
	v_lshl_add_u64 v[190:191], s[2:3], 0, v[176:177]
	s_add_i32 m0, s58, 0xe000
	s_nop 0
	global_load_lds_dwordx4 v[190:191], off
	s_waitcnt vmcnt(8)
	s_waitcnt lgkmcnt(0)
	s_barrier
	s_setprio 1
	s_waitcnt lgkmcnt(0)
	v_mfma_scale_f32_16x16x128_f8f6f4 v[158:161], v[18:25], v[182:189], v[158:161], v206, v207 op_sel_hi:[0,0,0]
	v_mfma_scale_f32_16x16x128_f8f6f4 v[154:157], v[26:33], v[182:189], v[154:157], v206, v207 op_sel_hi:[0,0,0]
	v_mfma_scale_f32_16x16x128_f8f6f4 v[142:145], v[18:25], v[212:219], v[142:145], v206, v207 op_sel_hi:[0,0,0]
	v_mfma_scale_f32_16x16x128_f8f6f4 v[138:141], v[26:33], v[212:219], v[138:141], v206, v207 op_sel_hi:[0,0,0]
	v_mfma_scale_f32_16x16x128_f8f6f4 v[126:129], v[18:25], v[220:227], v[126:129], v206, v207 op_sel_hi:[0,0,0]
	v_mfma_scale_f32_16x16x128_f8f6f4 v[122:125], v[26:33], v[220:227], v[122:125], v206, v207 op_sel_hi:[0,0,0]
	v_mfma_scale_f32_16x16x128_f8f6f4 v[110:113], v[18:25], v[228:235], v[110:113], v206, v207 op_sel_hi:[0,0,0]
	v_mfma_scale_f32_16x16x128_f8f6f4 v[106:109], v[26:33], v[228:235], v[106:109], v206, v207 op_sel_hi:[0,0,0]
	v_mfma_scale_f32_16x16x128_f8f6f4 v[150:153], v[2:9], v[182:189], v[150:153], v206, v207 op_sel_hi:[0,0,0]
	v_mfma_scale_f32_16x16x128_f8f6f4 v[146:149], v[10:17], v[182:189], v[146:149], v206, v207 op_sel_hi:[0,0,0]
	v_mfma_scale_f32_16x16x128_f8f6f4 v[134:137], v[2:9], v[212:219], v[134:137], v206, v207 op_sel_hi:[0,0,0]
	v_mfma_scale_f32_16x16x128_f8f6f4 v[130:133], v[10:17], v[212:219], v[130:133], v206, v207 op_sel_hi:[0,0,0]
	v_mfma_scale_f32_16x16x128_f8f6f4 v[118:121], v[2:9], v[220:227], v[118:121], v206, v207 op_sel_hi:[0,0,0]
	v_mfma_scale_f32_16x16x128_f8f6f4 v[114:117], v[10:17], v[220:227], v[114:117], v206, v207 op_sel_hi:[0,0,0]
	v_mfma_scale_f32_16x16x128_f8f6f4 v[102:105], v[2:9], v[228:235], v[102:105], v206, v207 op_sel_hi:[0,0,0]
	v_mfma_scale_f32_16x16x128_f8f6f4 v[98:101], v[10:17], v[228:235], v[98:101], v206, v207 op_sel_hi:[0,0,0]
	s_barrier
	s_setprio 0
	s_add_i32 s0, s76, s57
	v_lshl_add_u64 v[182:183], s[50:51], 0, v[164:165]
	s_mov_b32 m0, s0
	ds_read_b128 v[212:215], v205 offset:16384
	ds_read_b128 v[216:219], v205 offset:17408
	ds_read_b128 v[220:223], v205 offset:18432
	ds_read_b128 v[224:227], v205 offset:19456
	ds_read_b128 v[228:231], v205 offset:20480
	ds_read_b128 v[232:235], v205 offset:21504
	ds_read_b128 v[236:239], v205 offset:22528
	ds_read_b128 v[240:243], v205 offset:23552
	global_load_lds_dwordx4 v[182:183], off
	s_add_i32 m0, s0, 0x2000
	v_lshl_add_u64 v[184:185], s[50:51], 0, v[168:169]
	s_add_u32 s50, s50, s16
	s_addc_u32 s51, s51, s17
	s_add_i32 s0, s77, s57
	global_load_lds_dwordx4 v[184:185], off
	v_lshl_add_u64 v[186:187], s[50:51], 0, v[164:165]
	s_mov_b32 m0, s0
	v_lshl_add_u64 v[188:189], s[50:51], 0, v[168:169]
	global_load_lds_dwordx4 v[186:187], off
	s_add_i32 m0, s0, 0x2000
	v_lshl_add_u64 v[190:191], s[48:49], 0, v[162:163]
	global_load_lds_dwordx4 v[188:189], off
	v_lshl_add_u64 v[192:193], s[48:49], 0, v[166:167]
	s_waitcnt vmcnt(6)
	s_waitcnt lgkmcnt(0)
	s_barrier
	s_setprio 1
	s_waitcnt lgkmcnt(0)
	v_mfma_scale_f32_16x16x128_f8f6f4 v[94:97], v[18:25], v[212:219], v[94:97], v206, v207 op_sel_hi:[0,0,0]
	v_mfma_scale_f32_16x16x128_f8f6f4 v[90:93], v[26:33], v[212:219], v[90:93], v206, v207 op_sel_hi:[0,0,0]
	v_mfma_scale_f32_16x16x128_f8f6f4 v[78:81], v[18:25], v[220:227], v[78:81], v206, v207 op_sel_hi:[0,0,0]
	v_mfma_scale_f32_16x16x128_f8f6f4 v[74:77], v[26:33], v[220:227], v[74:77], v206, v207 op_sel_hi:[0,0,0]
	v_mfma_scale_f32_16x16x128_f8f6f4 v[62:65], v[18:25], v[228:235], v[62:65], v206, v207 op_sel_hi:[0,0,0]
	v_mfma_scale_f32_16x16x128_f8f6f4 v[58:61], v[26:33], v[228:235], v[58:61], v206, v207 op_sel_hi:[0,0,0]
	v_mfma_scale_f32_16x16x128_f8f6f4 v[46:49], v[18:25], v[236:243], v[46:49], v206, v207 op_sel_hi:[0,0,0]
	v_mfma_scale_f32_16x16x128_f8f6f4 v[42:45], v[26:33], v[236:243], v[42:45], v206, v207 op_sel_hi:[0,0,0]
	v_mfma_scale_f32_16x16x128_f8f6f4 v[86:89], v[2:9], v[212:219], v[86:89], v206, v207 op_sel_hi:[0,0,0]
	v_mfma_scale_f32_16x16x128_f8f6f4 v[82:85], v[10:17], v[212:219], v[82:85], v206, v207 op_sel_hi:[0,0,0]
	v_mfma_scale_f32_16x16x128_f8f6f4 v[70:73], v[2:9], v[220:227], v[70:73], v206, v207 op_sel_hi:[0,0,0]
	v_mfma_scale_f32_16x16x128_f8f6f4 v[66:69], v[10:17], v[220:227], v[66:69], v206, v207 op_sel_hi:[0,0,0]
	v_mfma_scale_f32_16x16x128_f8f6f4 v[54:57], v[2:9], v[228:235], v[54:57], v206, v207 op_sel_hi:[0,0,0]
	v_mfma_scale_f32_16x16x128_f8f6f4 v[50:53], v[10:17], v[228:235], v[50:53], v206, v207 op_sel_hi:[0,0,0]
	v_mfma_scale_f32_16x16x128_f8f6f4 v[38:41], v[2:9], v[236:243], v[38:41], v206, v207 op_sel_hi:[0,0,0]
	v_mfma_scale_f32_16x16x128_f8f6f4 v[34:37], v[10:17], v[236:243], v[34:37], v206, v207 op_sel_hi:[0,0,0]
	s_barrier
; #define PG8_STAGE(bufoff, gbase, voff) do { _Pragma("unroll") for (int _i = 0; _i < 2; ++_i) \
;         __builtin_amdgcn_global_load_lds((const unsigned*)((const char*)(gbase) + (voff)[_i]), (PG8_LAS unsigned*)(lds + (bufoff) + ldsw + _i * 8192), 16, 0, 0); } while (0)
; #define PG8_LDA(dst, b, h) do { _Pragma("unroll") for (int m = 0; m < 4; ++m) { const bf16x8 f0_ = *(const PG8_LAS bf16x8*)(lds + PG8_SA(b, h) + aoff + m * 2048), f1_ = *(const PG8_LAS bf16x8*)(lds + PG8_SA(b, h) + aoff + m * 2048 + 1024); dst[m].set(f0_, f1_); } } while (0)
; #define PG8_LDB(dst, b, h) do { _Pragma("unroll") for (int n = 0; n < 2; ++n) { const bf16x8 f0_ = *(const PG8_LAS bf16x8*)(lds + PG8_SB(b, h) + boff + n * 2048), f1_ = *(const PG8_LAS bf16x8*)(lds + PG8_SB(b, h) + boff + n * 2048 + 1024); dst[n].set(f0_, f1_); } } while (0)
; #define PG8_WAIT_V(n) asm volatile("s_waitcnt vmcnt(" #n ")" ::: "memory")
; #define PG8_WAIT_L(n) asm volatile("s_waitcnt lgkmcnt(" #n ")" ::: "memory")
; #define PG8_BAR __builtin_amdgcn_s_barrier()
; #define PG8_SCHED __builtin_amdgcn_sched_barrier(0)
; template <class Epi, class Sched, bool ALIGN_EPI = false, bool SP2 = false>
; __device__ __forceinline__ void gemm_phase(PG8_LAS unsigned char* lds, const Gemm g, const Sched& S, const Epi& E) {
;     ...
;         for (int t = 0; t < nt; t += 2) {
;             if constexpr (Epi::MIDK) { if (t == (nt >> 1)) E.mid(acc, cur, wr, wc, fr, fq); }
;             const bool last = (t == nt - 2);
;             const char* a1 = cA + (size_t)(t + 1) * kstep;
;             const char* a2 = last ? nA : cA + (size_t)(t + 2) * kstep; const char* b2 = last ? nB : cB + (size_t)(t + 2) * kstep;
;     ...
;             PG8_LDB(B0, 1, 0); PG8_LDB(B1, 1, 1); PG8_SCHED; PG8_LDA(At, 1, 0); PG8_STAGE(PG8_SA(0, 1), a2 + hstep, voffA);
;             PG8_WAIT_V(8); PG8_WAIT_L(0); PG8_BAR; PG8_MMA(0, 0, At, B0); PG8_MMA(0, 1, At, B1); PG8_BAR; PG8_SCHED;
;             PG8_LDA(At, 1, 1); PG8_STAGE(PG8_SB(1, 0), b3, voffB); PG8_STAGE(PG8_SB(1, 1), b3 + hstepB, voffB); PG8_STAGE(PG8_SA(1, 0), a3, voffA);
;             PG8_WAIT_V(8); PG8_WAIT_L(0); PG8_BAR; PG8_MMA(1, 0, At, B0); PG8_MMA(1, 1, At, B1); PG8_BAR; PG8_SCHED;
	s_setprio 0
	s_add_i32 s0, 0, 0x18000
	s_add_i32 s1, 0, 0x1c000
	v_add_u32_e32 v14, s0, v194
	v_add_u32_e32 v30, s1, v194
	ds_read_b128 v[2:5], v14
	ds_read_b128 v[6:9], v14 offset:1024
	ds_read_b128 v[10:13], v14 offset:2048
	ds_read_b128 v[14:17], v14 offset:3072
	ds_read_b128 v[18:21], v30
	ds_read_b128 v[22:25], v30 offset:1024
	ds_read_b128 v[26:29], v30 offset:2048
	ds_read_b128 v[30:33], v30 offset:3072
	s_add_u32 s48, s48, s14
	s_addc_u32 s49, s49, s15
	s_mov_b32 m0, s61
	v_lshl_add_u64 v[244:245], s[48:49], 0, v[162:163]
	ds_read_b128 v[212:215], v205 offset:32768
	ds_read_b128 v[216:219], v205 offset:33792
	ds_read_b128 v[220:223], v205 offset:34816
	ds_read_b128 v[224:227], v205 offset:35840
	ds_read_b128 v[228:231], v205 offset:36864
	ds_read_b128 v[232:235], v205 offset:37888
	ds_read_b128 v[236:239], v205 offset:38912
	ds_read_b128 v[240:243], v205 offset:39936
	s_mov_b32 m0, s58
	s_nop 0
	global_load_lds_dwordx4 v[190:191], off
	s_mov_b32 m0, s59
	s_nop 0
	global_load_lds_dwordx4 v[192:193], off
	s_mov_b32 m0, s61
	s_nop 0
	global_load_lds_dwordx4 v[244:245], off
	v_lshl_add_u64 v[244:245], s[48:49], 0, v[166:167]
	s_mov_b32 m0, s63
	s_nop 0
	global_load_lds_dwordx4 v[244:245], off
	s_waitcnt vmcnt(8)
	s_waitcnt lgkmcnt(0)
	s_barrier
	s_setprio 1
	s_waitcnt lgkmcnt(0)
	v_mfma_scale_f32_16x16x128_f8f6f4 v[158:161], v[2:9], v[212:219], v[158:161], v206, v207 op_sel_hi:[0,0,0]
	v_mfma_scale_f32_16x16x128_f8f6f4 v[154:157], v[10:17], v[212:219], v[154:157], v206, v207 op_sel_hi:[0,0,0]
	v_mfma_scale_f32_16x16x128_f8f6f4 v[142:145], v[2:9], v[220:227], v[142:145], v206, v207 op_sel_hi:[0,0,0]
	v_mfma_scale_f32_16x16x128_f8f6f4 v[138:141], v[10:17], v[220:227], v[138:141], v206, v207 op_sel_hi:[0,0,0]
	v_mfma_scale_f32_16x16x128_f8f6f4 v[126:129], v[2:9], v[228:235], v[126:129], v206, v207 op_sel_hi:[0,0,0]
	v_mfma_scale_f32_16x16x128_f8f6f4 v[122:125], v[10:17], v[228:235], v[122:125], v206, v207 op_sel_hi:[0,0,0]
	v_mfma_scale_f32_16x16x128_f8f6f4 v[110:113], v[2:9], v[236:243], v[110:113], v206, v207 op_sel_hi:[0,0,0]
	v_mfma_scale_f32_16x16x128_f8f6f4 v[106:109], v[10:17], v[236:243], v[106:109], v206, v207 op_sel_hi:[0,0,0]
	v_mfma_scale_f32_16x16x128_f8f6f4 v[150:153], v[18:25], v[212:219], v[150:153], v206, v207 op_sel_hi:[0,0,0]
	v_mfma_scale_f32_16x16x128_f8f6f4 v[146:149], v[26:33], v[212:219], v[146:149], v206, v207 op_sel_hi:[0,0,0]
	v_mfma_scale_f32_16x16x128_f8f6f4 v[134:137], v[18:25], v[220:227], v[134:137], v206, v207 op_sel_hi:[0,0,0]
	v_mfma_scale_f32_16x16x128_f8f6f4 v[130:133], v[26:33], v[220:227], v[130:133], v206, v207 op_sel_hi:[0,0,0]
	v_mfma_scale_f32_16x16x128_f8f6f4 v[118:121], v[18:25], v[228:235], v[118:121], v206, v207 op_sel_hi:[0,0,0]
	v_mfma_scale_f32_16x16x128_f8f6f4 v[114:117], v[26:33], v[228:235], v[114:117], v206, v207 op_sel_hi:[0,0,0]
	v_mfma_scale_f32_16x16x128_f8f6f4 v[102:105], v[18:25], v[236:243], v[102:105], v206, v207 op_sel_hi:[0,0,0]
	v_mfma_scale_f32_16x16x128_f8f6f4 v[98:101], v[26:33], v[236:243], v[98:101], v206, v207 op_sel_hi:[0,0,0]
	s_barrier
	s_setprio 0
	s_add_i32 s0, s0, s57
	v_lshl_add_u64 v[182:183], v[182:183], 0, s[36:37]
	s_mov_b32 m0, s0
	ds_read_b128 v[212:215], v205 offset:49152
	ds_read_b128 v[216:219], v205 offset:50176
	ds_read_b128 v[220:223], v205 offset:51200
	ds_read_b128 v[224:227], v205 offset:52224
	ds_read_b128 v[228:231], v205 offset:53248
	ds_read_b128 v[232:235], v205 offset:54272
	ds_read_b128 v[236:239], v205 offset:55296
	ds_read_b128 v[240:243], v205 offset:56320
	global_load_lds_dwordx4 v[182:183], off
	v_lshl_add_u64 v[182:183], v[184:185], 0, s[36:37]
	s_add_i32 m0, s0, 0x2000
	s_add_i32 s0, s1, s57
	global_load_lds_dwordx4 v[182:183], off
	v_lshl_add_u64 v[182:183], v[186:187], 0, s[36:37]
	s_mov_b32 m0, s0
	s_nop 0
	global_load_lds_dwordx4 v[182:183], off
	v_lshl_add_u64 v[182:183], v[188:189], 0, s[36:37]
	s_add_i32 m0, s0, 0x2000
	s_nop 0
	global_load_lds_dwordx4 v[182:183], off
	s_cmp_ge_i32 s53, s69
	s_cbranch_scc0 .Lkr0_b
	v_lshl_add_u64 v[182:183], v[190:191], 0, s[36:37]
	s_mov_b32 m0, s66
	s_nop 0
	global_load_lds_dwordx4 v[182:183], off
	v_lshl_add_u64 v[182:183], v[192:193], 0, s[36:37]
	s_mov_b32 m0, s67
	s_nop 0
	global_load_lds_dwordx4 v[182:183], off
.Lkr0_b:
	s_waitcnt vmcnt(6)
	s_waitcnt lgkmcnt(0)
	s_barrier
	s_setprio 1
	s_waitcnt lgkmcnt(0)
	v_mfma_scale_f32_16x16x128_f8f6f4 v[94:97], v[2:9], v[212:219], v[94:97], v206, v207 op_sel_hi:[0,0,0]
	v_mfma_scale_f32_16x16x128_f8f6f4 v[90:93], v[10:17], v[212:219], v[90:93], v206, v207 op_sel_hi:[0,0,0]
	v_mfma_scale_f32_16x16x128_f8f6f4 v[78:81], v[2:9], v[220:227], v[78:81], v206, v207 op_sel_hi:[0,0,0]
	v_mfma_scale_f32_16x16x128_f8f6f4 v[74:77], v[10:17], v[220:227], v[74:77], v206, v207 op_sel_hi:[0,0,0]
	v_mfma_scale_f32_16x16x128_f8f6f4 v[62:65], v[2:9], v[228:235], v[62:65], v206, v207 op_sel_hi:[0,0,0]
	v_mfma_scale_f32_16x16x128_f8f6f4 v[58:61], v[10:17], v[228:235], v[58:61], v206, v207 op_sel_hi:[0,0,0]
	v_mfma_scale_f32_16x16x128_f8f6f4 v[46:49], v[2:9], v[236:243], v[46:49], v206, v207 op_sel_hi:[0,0,0]
	v_mfma_scale_f32_16x16x128_f8f6f4 v[42:45], v[10:17], v[236:243], v[42:45], v206, v207 op_sel_hi:[0,0,0]
	v_mfma_scale_f32_16x16x128_f8f6f4 v[86:89], v[18:25], v[212:219], v[86:89], v206, v207 op_sel_hi:[0,0,0]
	v_mfma_scale_f32_16x16x128_f8f6f4 v[82:85], v[26:33], v[212:219], v[82:85], v206, v207 op_sel_hi:[0,0,0]
	v_mfma_scale_f32_16x16x128_f8f6f4 v[70:73], v[18:25], v[220:227], v[70:73], v206, v207 op_sel_hi:[0,0,0]
	v_mfma_scale_f32_16x16x128_f8f6f4 v[66:69], v[26:33], v[220:227], v[66:69], v206, v207 op_sel_hi:[0,0,0]
	v_mfma_scale_f32_16x16x128_f8f6f4 v[54:57], v[18:25], v[228:235], v[54:57], v206, v207 op_sel_hi:[0,0,0]
	v_mfma_scale_f32_16x16x128_f8f6f4 v[50:53], v[26:33], v[228:235], v[50:53], v206, v207 op_sel_hi:[0,0,0]
	v_mfma_scale_f32_16x16x128_f8f6f4 v[38:41], v[18:25], v[236:243], v[38:41], v206, v207 op_sel_hi:[0,0,0]
	v_mfma_scale_f32_16x16x128_f8f6f4 v[34:37], v[26:33], v[236:243], v[34:37], v206, v207 op_sel_hi:[0,0,0]
	s_barrier
	s_setprio 0
	s_add_u32 s2, s2, 0x100
	s_addc_u32 s3, s3, 0
	s_add_u32 s20, s20, 0x100
	s_addc_u32 s52, s52, 0
	s_cmp_ge_i32 s53, s69
	s_cselect_b32 s99, 0, 1
	s_mov_b32 s48, s53
	s_cbranch_scc0 .LBB0_204

; #define PG8_STAGE(bufoff, gbase, voff) do { _Pragma("unroll") for (int _i = 0; _i < 2; ++_i) \
;         __builtin_amdgcn_global_load_lds((const unsigned*)((const char*)(gbase) + (voff)[_i]), (PG8_LAS unsigned*)(lds + (bufoff) + ldsw + _i * 8192), 16, 0, 0); } while (0)
; #define PG8_LDA(dst, b, h) do { _Pragma("unroll") for (int m = 0; m < 4; ++m) { const bf16x8 f0_ = *(const PG8_LAS bf16x8*)(lds + PG8_SA(b, h) + aoff + m * 2048), f1_ = *(const PG8_LAS bf16x8*)(lds + PG8_SA(b, h) + aoff + m * 2048 + 1024); dst[m].set(f0_, f1_); } } while (0)
; #define PG8_LDB(dst, b, h) do { _Pragma("unroll") for (int n = 0; n < 2; ++n) { const bf16x8 f0_ = *(const PG8_LAS bf16x8*)(lds + PG8_SB(b, h) + boff + n * 2048), f1_ = *(const PG8_LAS bf16x8*)(lds + PG8_SB(b, h) + boff + n * 2048 + 1024); dst[n].set(f0_, f1_); } } while (0)
; #define PG8_WAIT_V(n) asm volatile("s_waitcnt vmcnt(" #n ")" ::: "memory")
; #define PG8_WAIT_L(n) asm volatile("s_waitcnt lgkmcnt(" #n ")" ::: "memory")
; #define PG8_BAR __builtin_amdgcn_s_barrier()
; #define PG8_SCHED __builtin_amdgcn_sched_barrier(0)
; template <class Epi, class Sched, bool ALIGN_EPI = false, bool SP2 = false>
; __device__ __forceinline__ void gemm_phase(PG8_LAS unsigned char* lds, const Gemm g, const Sched& S, const Epi& E) {
;     ...
;             const bool last = (t == nt - 2);
;             const char* a1 = cA + (size_t)(t + 1) * kstep;
;             const char* a2 = last ? nA : cA + (size_t)(t + 2) * kstep; const char* b2 = last ? nB : cB + (size_t)(t + 2) * kstep;
;             const char* a3 = a2 + kstep; const char* b3 = b2 + kstep;
;             if (last && has_next) S.a_ready(nxt);
;             if constexpr (SP2) {
;             PG8_LDB(B0, 0, 0); PG8_LDB(B1, 0, 1); PG8_SCHED; PG8_LDA(At, 0, 0); PG8_STAGE(PG8_SA(1, 1), a1 + hstep, voffA);
;             PG8_WAIT_V(8); PG8_WAIT_L(0); PG8_BAR; PG8_MMA(0, 0, At, B0); PG8_MMA(0, 1, At, B1); PG8_BAR; PG8_SCHED;
;             PG8_LDA(At, 0, 1); PG8_STAGE(PG8_SB(0, 0), b2, voffB); PG8_STAGE(PG8_SB(0, 1), b2 + hstepB, voffB); PG8_STAGE(PG8_SA(0, 0), a2, voffA);
;             PG8_WAIT_V(8); PG8_WAIT_L(0); PG8_BAR; PG8_MMA(1, 0, At, B0); PG8_MMA(1, 1, At, B1); PG8_BAR; PG8_SCHED;
.LBB0_984:
	s_add_i32 s75, s42, 2
	v_add_u32_e32 v186, s59, v173
	v_add_u32_e32 v202, s61, v173
	s_add_u32 s0, s38, s40
	ds_read_b128 v[168:171], v186
	ds_read_b128 v[178:181], v186 offset:1024
	ds_read_b128 v[182:185], v186 offset:2048
	ds_read_b128 v[186:189], v186 offset:3072
	ds_read_b128 v[190:193], v202
	ds_read_b128 v[194:197], v202 offset:1024
	ds_read_b128 v[198:201], v202 offset:2048
	ds_read_b128 v[202:205], v202 offset:3072
	s_addc_u32 s1, s39, s41
	s_add_u32 s0, s0, 0x100
	s_addc_u32 s1, s1, 0
	s_add_u32 s33, s73, s40
	s_addc_u32 s76, s74, s41
	s_cmp_eq_u32 s57, s42
	s_cselect_b32 s43, s3, s1
	s_cselect_b32 s42, s2, s0
	s_cselect_b32 s1, s37, s76
	s_cselect_b32 s0, s36, s33
	v_lshl_add_u64 v[240:241], v[164:165], 0, s[40:41]
	s_add_i32 m0, s47, 0xc000
	ds_read_b128 v[206:209], v176
	ds_read_b128 v[212:215], v176 offset:1024
	ds_read_b128 v[216:219], v176 offset:2048
	ds_read_b128 v[220:223], v176 offset:3072
	ds_read_b128 v[224:227], v176 offset:4096
	ds_read_b128 v[228:231], v176 offset:5120
	ds_read_b128 v[232:235], v176 offset:6144
	ds_read_b128 v[236:239], v176 offset:7168
	global_load_lds_dwordx4 v[240:241], off
	v_lshl_add_u64 v[240:241], v[166:167], 0, s[40:41]
	s_add_i32 m0, s47, 0xe000
	s_nop 0
	global_load_lds_dwordx4 v[240:241], off
	s_waitcnt vmcnt(8)
	s_waitcnt lgkmcnt(0)
	s_barrier
	s_setprio 1
	s_waitcnt lgkmcnt(0)
	v_mfma_f32_16x16x32_bf16 v[126:129], v[168:171], v[206:209], v[126:129]
	v_mfma_f32_16x16x32_bf16 v[122:125], v[182:185], v[206:209], v[122:125]
	v_mfma_f32_16x16x32_bf16 v[110:113], v[168:171], v[216:219], v[110:113]
	v_mfma_f32_16x16x32_bf16 v[106:109], v[182:185], v[216:219], v[106:109]
	v_mfma_f32_16x16x32_bf16 v[94:97], v[168:171], v[224:227], v[94:97]
	v_mfma_f32_16x16x32_bf16 v[90:93], v[182:185], v[224:227], v[90:93]
	v_mfma_f32_16x16x32_bf16 v[78:81], v[168:171], v[232:235], v[78:81]
	v_mfma_f32_16x16x32_bf16 v[74:77], v[182:185], v[232:235], v[74:77]
	v_mfma_f32_16x16x32_bf16 v[126:129], v[178:181], v[212:215], v[126:129]
	v_mfma_f32_16x16x32_bf16 v[122:125], v[186:189], v[212:215], v[122:125]
	v_mfma_f32_16x16x32_bf16 v[110:113], v[178:181], v[220:223], v[110:113]
	v_mfma_f32_16x16x32_bf16 v[106:109], v[186:189], v[220:223], v[106:109]
	v_mfma_f32_16x16x32_bf16 v[94:97], v[178:181], v[228:231], v[94:97]
	v_mfma_f32_16x16x32_bf16 v[90:93], v[186:189], v[228:231], v[90:93]
	v_mfma_f32_16x16x32_bf16 v[78:81], v[178:181], v[236:239], v[78:81]
	v_mfma_f32_16x16x32_bf16 v[74:77], v[186:189], v[236:239], v[74:77]
	v_mfma_f32_16x16x32_bf16 v[118:121], v[190:193], v[206:209], v[118:121]
	v_mfma_f32_16x16x32_bf16 v[114:117], v[198:201], v[206:209], v[114:117]
	v_mfma_f32_16x16x32_bf16 v[102:105], v[190:193], v[216:219], v[102:105]
	v_mfma_f32_16x16x32_bf16 v[98:101], v[198:201], v[216:219], v[98:101]
	v_mfma_f32_16x16x32_bf16 v[86:89], v[190:193], v[224:227], v[86:89]
	v_mfma_f32_16x16x32_bf16 v[82:85], v[198:201], v[224:227], v[82:85]
	v_mfma_f32_16x16x32_bf16 v[70:73], v[190:193], v[232:235], v[70:73]
	v_mfma_f32_16x16x32_bf16 v[66:69], v[198:201], v[232:235], v[66:69]
	v_mfma_f32_16x16x32_bf16 v[118:121], v[194:197], v[212:215], v[118:121]
	v_mfma_f32_16x16x32_bf16 v[114:117], v[202:205], v[212:215], v[114:117]
	v_mfma_f32_16x16x32_bf16 v[102:105], v[194:197], v[220:223], v[102:105]
	v_mfma_f32_16x16x32_bf16 v[98:101], v[202:205], v[220:223], v[98:101]
	v_mfma_f32_16x16x32_bf16 v[86:89], v[194:197], v[228:231], v[86:89]
	v_mfma_f32_16x16x32_bf16 v[82:85], v[202:205], v[228:231], v[82:85]
	v_mfma_f32_16x16x32_bf16 v[70:73], v[194:197], v[236:239], v[70:73]
	v_mfma_f32_16x16x32_bf16 v[66:69], v[202:205], v[236:239], v[66:69]
	s_barrier
	s_setprio 0
	s_add_i32 s33, s59, s46
	v_lshl_add_u64 v[240:241], s[0:1], 0, v[132:133]
	s_mov_b32 m0, s33
	ds_read_b128 v[206:209], v176 offset:16384
	ds_read_b128 v[212:215], v176 offset:17408
	ds_read_b128 v[216:219], v176 offset:18432
	ds_read_b128 v[220:223], v176 offset:19456
	ds_read_b128 v[224:227], v176 offset:20480
	ds_read_b128 v[228:231], v176 offset:21504
	ds_read_b128 v[232:235], v176 offset:22528
	ds_read_b128 v[236:239], v176 offset:23552
	global_load_lds_dwordx4 v[240:241], off
	s_add_i32 m0, s33, 0x2000
	v_lshl_add_u64 v[242:243], s[0:1], 0, v[136:137]
	s_add_u32 s0, s0, s14
	s_addc_u32 s1, s1, s15
	s_add_i32 s33, s61, s46
	global_load_lds_dwordx4 v[242:243], off
	v_lshl_add_u64 v[244:245], s[0:1], 0, v[132:133]
	s_mov_b32 m0, s33
	v_lshl_add_u64 v[246:247], s[0:1], 0, v[136:137]
	global_load_lds_dwordx4 v[244:245], off
	s_add_i32 m0, s33, 0x2000
	v_lshl_add_u64 v[248:249], s[42:43], 0, v[130:131]
	global_load_lds_dwordx4 v[246:247], off
	v_lshl_add_u64 v[250:251], s[42:43], 0, v[134:135]
	s_waitcnt vmcnt(6)
	s_waitcnt lgkmcnt(0)
	s_barrier
; #define PG8_STAGE(bufoff, gbase, voff) do { _Pragma("unroll") for (int _i = 0; _i < 2; ++_i) \
;         __builtin_amdgcn_global_load_lds((const unsigned*)((const char*)(gbase) + (voff)[_i]), (PG8_LAS unsigned*)(lds + (bufoff) + ldsw + _i * 8192), 16, 0, 0); } while (0)
; #define PG8_LDA(dst, b, h) do { _Pragma("unroll") for (int m = 0; m < 4; ++m) { const bf16x8 f0_ = *(const PG8_LAS bf16x8*)(lds + PG8_SA(b, h) + aoff + m * 2048), f1_ = *(const PG8_LAS bf16x8*)(lds + PG8_SA(b, h) + aoff + m * 2048 + 1024); dst[m].set(f0_, f1_); } } while (0)
; #define PG8_LDB(dst, b, h) do { _Pragma("unroll") for (int n = 0; n < 2; ++n) { const bf16x8 f0_ = *(const PG8_LAS bf16x8*)(lds + PG8_SB(b, h) + boff + n * 2048), f1_ = *(const PG8_LAS bf16x8*)(lds + PG8_SB(b, h) + boff + n * 2048 + 1024); dst[n].set(f0_, f1_); } } while (0)
; #define PG8_WAIT_V(n) asm volatile("s_waitcnt vmcnt(" #n ")" ::: "memory")
; #define PG8_WAIT_L(n) asm volatile("s_waitcnt lgkmcnt(" #n ")" ::: "memory")
; #define PG8_BAR __builtin_amdgcn_s_barrier()
; #define PG8_SCHED __builtin_amdgcn_sched_barrier(0)
; template <class Epi, class Sched, bool ALIGN_EPI = false, bool SP2 = false>
; __device__ __forceinline__ void gemm_phase(PG8_LAS unsigned char* lds, const Gemm g, const Sched& S, const Epi& E) {
;     ...
;             PG8_WAIT_V(8); PG8_WAIT_L(0); PG8_BAR; PG8_MMA(1, 0, At, B0); PG8_MMA(1, 1, At, B1); PG8_BAR; PG8_SCHED;
;             PG8_LDB(B0, 1, 0); PG8_LDB(B1, 1, 1); PG8_SCHED; PG8_LDA(At, 1, 0); PG8_STAGE(PG8_SA(0, 1), a2 + hstep, voffA);
;             PG8_WAIT_V(8); PG8_WAIT_L(0); PG8_BAR; PG8_MMA(0, 0, At, B0); PG8_MMA(0, 1, At, B1); PG8_BAR; PG8_SCHED;
	s_setprio 1
	s_waitcnt lgkmcnt(0)
	v_mfma_f32_16x16x32_bf16 v[62:65], v[168:171], v[206:209], v[62:65]
	v_mfma_f32_16x16x32_bf16 v[58:61], v[182:185], v[206:209], v[58:61]
	v_mfma_f32_16x16x32_bf16 v[46:49], v[168:171], v[216:219], v[46:49]
	v_mfma_f32_16x16x32_bf16 v[42:45], v[182:185], v[216:219], v[42:45]
	v_mfma_f32_16x16x32_bf16 v[30:33], v[168:171], v[224:227], v[30:33]
	v_mfma_f32_16x16x32_bf16 v[26:29], v[182:185], v[224:227], v[26:29]
	v_mfma_f32_16x16x32_bf16 v[14:17], v[168:171], v[232:235], v[14:17]
	v_mfma_f32_16x16x32_bf16 v[10:13], v[182:185], v[232:235], v[10:13]
	v_mfma_f32_16x16x32_bf16 v[62:65], v[178:181], v[212:215], v[62:65]
	v_mfma_f32_16x16x32_bf16 v[58:61], v[186:189], v[212:215], v[58:61]
	v_mfma_f32_16x16x32_bf16 v[46:49], v[178:181], v[220:223], v[46:49]
	v_mfma_f32_16x16x32_bf16 v[42:45], v[186:189], v[220:223], v[42:45]
	v_mfma_f32_16x16x32_bf16 v[30:33], v[178:181], v[228:231], v[30:33]
	v_mfma_f32_16x16x32_bf16 v[26:29], v[186:189], v[228:231], v[26:29]
	v_mfma_f32_16x16x32_bf16 v[14:17], v[178:181], v[236:239], v[14:17]
	v_mfma_f32_16x16x32_bf16 v[10:13], v[186:189], v[236:239], v[10:13]
	v_mfma_f32_16x16x32_bf16 v[54:57], v[190:193], v[206:209], v[54:57]
	v_mfma_f32_16x16x32_bf16 v[50:53], v[198:201], v[206:209], v[50:53]
	v_mfma_f32_16x16x32_bf16 v[38:41], v[190:193], v[216:219], v[38:41]
	v_mfma_f32_16x16x32_bf16 v[34:37], v[198:201], v[216:219], v[34:37]
	v_mfma_f32_16x16x32_bf16 v[22:25], v[190:193], v[224:227], v[22:25]
	v_mfma_f32_16x16x32_bf16 v[18:21], v[198:201], v[224:227], v[18:21]
	v_mfma_f32_16x16x32_bf16 v[6:9], v[190:193], v[232:235], v[6:9]
	v_mfma_f32_16x16x32_bf16 v[2:5], v[198:201], v[232:235], v[2:5]
	v_mfma_f32_16x16x32_bf16 v[54:57], v[194:197], v[212:215], v[54:57]
	v_mfma_f32_16x16x32_bf16 v[50:53], v[202:205], v[212:215], v[50:53]
	v_mfma_f32_16x16x32_bf16 v[38:41], v[194:197], v[220:223], v[38:41]
	v_mfma_f32_16x16x32_bf16 v[34:37], v[202:205], v[220:223], v[34:37]
	v_mfma_f32_16x16x32_bf16 v[22:25], v[194:197], v[228:231], v[22:25]
	v_mfma_f32_16x16x32_bf16 v[18:21], v[202:205], v[228:231], v[18:21]
	v_mfma_f32_16x16x32_bf16 v[6:9], v[194:197], v[236:239], v[6:9]
	v_mfma_f32_16x16x32_bf16 v[2:5], v[202:205], v[236:239], v[2:5]
	s_barrier
	s_setprio 0
	s_add_i32 s33, 0, 0x18000
	s_add_i32 s76, 0, 0x1c000
	v_add_u32_e32 v186, s33, v173
	v_add_u32_e32 v202, s76, v173
	ds_read_b128 v[168:171], v186
	ds_read_b128 v[178:181], v186 offset:1024
	ds_read_b128 v[182:185], v186 offset:2048
	ds_read_b128 v[186:189], v186 offset:3072
	ds_read_b128 v[190:193], v202
	ds_read_b128 v[194:197], v202 offset:1024
	ds_read_b128 v[198:201], v202 offset:2048
	ds_read_b128 v[202:205], v202 offset:3072
	s_add_u32 s0, s42, s12
	s_addc_u32 s1, s43, s13
	s_mov_b32 m0, s49
	v_lshl_add_u64 v[252:253], s[0:1], 0, v[130:131]
	ds_read_b128 v[206:209], v176 offset:32768
	ds_read_b128 v[212:215], v176 offset:33792
	ds_read_b128 v[216:219], v176 offset:34816
	ds_read_b128 v[220:223], v176 offset:35840
	ds_read_b128 v[224:227], v176 offset:36864
	ds_read_b128 v[228:231], v176 offset:37888
	ds_read_b128 v[232:235], v176 offset:38912
	ds_read_b128 v[236:239], v176 offset:39936
	s_mov_b32 m0, s47
	s_nop 0
	global_load_lds_dwordx4 v[248:249], off
	s_mov_b32 m0, s48
	s_nop 0
	global_load_lds_dwordx4 v[250:251], off
	s_mov_b32 m0, s49
	s_nop 0
	global_load_lds_dwordx4 v[252:253], off
	v_lshl_add_u64 v[252:253], s[0:1], 0, v[134:135]
	s_mov_b32 m0, s50
	s_nop 0
	global_load_lds_dwordx4 v[252:253], off
	s_waitcnt vmcnt(8)
	s_waitcnt lgkmcnt(0)
	s_barrier
; #define PG8_STAGE(bufoff, gbase, voff) do { _Pragma("unroll") for (int _i = 0; _i < 2; ++_i) \
;         __builtin_amdgcn_global_load_lds((const unsigned*)((const char*)(gbase) + (voff)[_i]), (PG8_LAS unsigned*)(lds + (bufoff) + ldsw + _i * 8192), 16, 0, 0); } while (0)
; #define PG8_LDA(dst, b, h) do { _Pragma("unroll") for (int m = 0; m < 4; ++m) { const bf16x8 f0_ = *(const PG8_LAS bf16x8*)(lds + PG8_SA(b, h) + aoff + m * 2048), f1_ = *(const PG8_LAS bf16x8*)(lds + PG8_SA(b, h) + aoff + m * 2048 + 1024); dst[m].set(f0_, f1_); } } while (0)
; #define PG8_WAIT_V(n) asm volatile("s_waitcnt vmcnt(" #n ")" ::: "memory")
; #define PG8_WAIT_L(n) asm volatile("s_waitcnt lgkmcnt(" #n ")" ::: "memory")
; #define PG8_BAR __builtin_amdgcn_s_barrier()
; #define PG8_SCHED __builtin_amdgcn_sched_barrier(0)
; template <class Epi, class Sched, bool ALIGN_EPI = false, bool SP2 = false>
; __device__ __forceinline__ void gemm_phase(PG8_LAS unsigned char* lds, const Gemm g, const Sched& S, const Epi& E) {
;     ...
;         for (int t = 0; t < nt; t += 2) {
;             if constexpr (Epi::MIDK) { if (t == (nt >> 1)) E.mid(acc, cur, wr, wc, fr, fq); }
;             const bool last = (t == nt - 2);
;             const char* a1 = cA + (size_t)(t + 1) * kstep;
;             const char* a2 = last ? nA : cA + (size_t)(t + 2) * kstep; const char* b2 = last ? nB : cB + (size_t)(t + 2) * kstep;
;     ...
;             PG8_WAIT_V(8); PG8_WAIT_L(0); PG8_BAR; PG8_MMA(0, 0, At, B0); PG8_MMA(0, 1, At, B1); PG8_BAR; PG8_SCHED;
;             PG8_LDA(At, 1, 1); PG8_STAGE(PG8_SB(1, 0), b3, voffB); PG8_STAGE(PG8_SB(1, 1), b3 + hstepB, voffB); PG8_STAGE(PG8_SA(1, 0), a3, voffA);
;             PG8_WAIT_V(8); PG8_WAIT_L(0); PG8_BAR; PG8_MMA(1, 0, At, B0); PG8_MMA(1, 1, At, B1); PG8_BAR; PG8_SCHED;
	s_setprio 1
	s_waitcnt lgkmcnt(0)
	v_mfma_f32_16x16x32_bf16 v[126:129], v[168:171], v[206:209], v[126:129]
	v_mfma_f32_16x16x32_bf16 v[122:125], v[182:185], v[206:209], v[122:125]
	v_mfma_f32_16x16x32_bf16 v[110:113], v[168:171], v[216:219], v[110:113]
	v_mfma_f32_16x16x32_bf16 v[106:109], v[182:185], v[216:219], v[106:109]
	v_mfma_f32_16x16x32_bf16 v[94:97], v[168:171], v[224:227], v[94:97]
	v_mfma_f32_16x16x32_bf16 v[90:93], v[182:185], v[224:227], v[90:93]
	v_mfma_f32_16x16x32_bf16 v[78:81], v[168:171], v[232:235], v[78:81]
	v_mfma_f32_16x16x32_bf16 v[74:77], v[182:185], v[232:235], v[74:77]
	v_mfma_f32_16x16x32_bf16 v[126:129], v[178:181], v[212:215], v[126:129]
	v_mfma_f32_16x16x32_bf16 v[122:125], v[186:189], v[212:215], v[122:125]
	v_mfma_f32_16x16x32_bf16 v[110:113], v[178:181], v[220:223], v[110:113]
	v_mfma_f32_16x16x32_bf16 v[106:109], v[186:189], v[220:223], v[106:109]
	v_mfma_f32_16x16x32_bf16 v[94:97], v[178:181], v[228:231], v[94:97]
	v_mfma_f32_16x16x32_bf16 v[90:93], v[186:189], v[228:231], v[90:93]
	v_mfma_f32_16x16x32_bf16 v[78:81], v[178:181], v[236:239], v[78:81]
	v_mfma_f32_16x16x32_bf16 v[74:77], v[186:189], v[236:239], v[74:77]
	v_mfma_f32_16x16x32_bf16 v[118:121], v[190:193], v[206:209], v[118:121]
	v_mfma_f32_16x16x32_bf16 v[114:117], v[198:201], v[206:209], v[114:117]
	v_mfma_f32_16x16x32_bf16 v[102:105], v[190:193], v[216:219], v[102:105]
	v_mfma_f32_16x16x32_bf16 v[98:101], v[198:201], v[216:219], v[98:101]
	v_mfma_f32_16x16x32_bf16 v[86:89], v[190:193], v[224:227], v[86:89]
	v_mfma_f32_16x16x32_bf16 v[82:85], v[198:201], v[224:227], v[82:85]
	v_mfma_f32_16x16x32_bf16 v[70:73], v[190:193], v[232:235], v[70:73]
	v_mfma_f32_16x16x32_bf16 v[66:69], v[198:201], v[232:235], v[66:69]
	v_mfma_f32_16x16x32_bf16 v[118:121], v[194:197], v[212:215], v[118:121]
	v_mfma_f32_16x16x32_bf16 v[114:117], v[202:205], v[212:215], v[114:117]
	v_mfma_f32_16x16x32_bf16 v[102:105], v[194:197], v[220:223], v[102:105]
	v_mfma_f32_16x16x32_bf16 v[98:101], v[202:205], v[220:223], v[98:101]
	v_mfma_f32_16x16x32_bf16 v[86:89], v[194:197], v[228:231], v[86:89]
	v_mfma_f32_16x16x32_bf16 v[82:85], v[202:205], v[228:231], v[82:85]
	v_mfma_f32_16x16x32_bf16 v[70:73], v[194:197], v[236:239], v[70:73]
	v_mfma_f32_16x16x32_bf16 v[66:69], v[202:205], v[236:239], v[66:69]
	s_barrier
	s_setprio 0
	s_add_i32 s0, s33, s46
	v_lshl_add_u64 v[240:241], v[240:241], 0, s[26:27]
	s_mov_b32 m0, s0
	ds_read_b128 v[206:209], v176 offset:49152
	ds_read_b128 v[212:215], v176 offset:50176
	ds_read_b128 v[216:219], v176 offset:51200
	ds_read_b128 v[220:223], v176 offset:52224
	ds_read_b128 v[224:227], v176 offset:53248
	ds_read_b128 v[228:231], v176 offset:54272
	ds_read_b128 v[232:235], v176 offset:55296
	ds_read_b128 v[236:239], v176 offset:56320
	global_load_lds_dwordx4 v[240:241], off
	v_lshl_add_u64 v[240:241], v[242:243], 0, s[26:27]
	s_add_i32 m0, s0, 0x2000
	s_add_i32 s0, s76, s46
	global_load_lds_dwordx4 v[240:241], off
	v_lshl_add_u64 v[240:241], v[244:245], 0, s[26:27]
	s_mov_b32 m0, s0
	s_nop 0
	global_load_lds_dwordx4 v[240:241], off
	v_lshl_add_u64 v[240:241], v[246:247], 0, s[26:27]
	s_add_i32 m0, s0, 0x2000
	s_nop 0
	global_load_lds_dwordx4 v[240:241], off
	v_lshl_add_u64 v[240:241], v[248:249], 0, s[26:27]
	s_mov_b32 m0, s52
	s_nop 0
	global_load_lds_dwordx4 v[240:241], off
	v_lshl_add_u64 v[240:241], v[250:251], 0, s[26:27]
	s_mov_b32 m0, s53
	s_nop 0
	global_load_lds_dwordx4 v[240:241], off
	s_waitcnt vmcnt(6)
	s_waitcnt lgkmcnt(0)
	s_barrier
	s_setprio 1
	s_waitcnt lgkmcnt(0)
	v_mfma_f32_16x16x32_bf16 v[62:65], v[168:171], v[206:209], v[62:65]
	v_mfma_f32_16x16x32_bf16 v[58:61], v[182:185], v[206:209], v[58:61]
	v_mfma_f32_16x16x32_bf16 v[46:49], v[168:171], v[216:219], v[46:49]
	v_mfma_f32_16x16x32_bf16 v[42:45], v[182:185], v[216:219], v[42:45]
	v_mfma_f32_16x16x32_bf16 v[30:33], v[168:171], v[224:227], v[30:33]
	v_mfma_f32_16x16x32_bf16 v[26:29], v[182:185], v[224:227], v[26:29]
	v_mfma_f32_16x16x32_bf16 v[14:17], v[168:171], v[232:235], v[14:17]
	v_mfma_f32_16x16x32_bf16 v[10:13], v[182:185], v[232:235], v[10:13]
	v_mfma_f32_16x16x32_bf16 v[62:65], v[178:181], v[212:215], v[62:65]
	v_mfma_f32_16x16x32_bf16 v[58:61], v[186:189], v[212:215], v[58:61]
	v_mfma_f32_16x16x32_bf16 v[46:49], v[178:181], v[220:223], v[46:49]
	v_mfma_f32_16x16x32_bf16 v[42:45], v[186:189], v[220:223], v[42:45]
	v_mfma_f32_16x16x32_bf16 v[30:33], v[178:181], v[228:231], v[30:33]
	v_mfma_f32_16x16x32_bf16 v[26:29], v[186:189], v[228:231], v[26:29]
	v_mfma_f32_16x16x32_bf16 v[14:17], v[178:181], v[236:239], v[14:17]
	v_mfma_f32_16x16x32_bf16 v[10:13], v[186:189], v[236:239], v[10:13]
	v_mfma_f32_16x16x32_bf16 v[54:57], v[190:193], v[206:209], v[54:57]
	v_mfma_f32_16x16x32_bf16 v[50:53], v[198:201], v[206:209], v[50:53]
	v_mfma_f32_16x16x32_bf16 v[38:41], v[190:193], v[216:219], v[38:41]
	v_mfma_f32_16x16x32_bf16 v[34:37], v[198:201], v[216:219], v[34:37]
	v_mfma_f32_16x16x32_bf16 v[22:25], v[190:193], v[224:227], v[22:25]
	v_mfma_f32_16x16x32_bf16 v[18:21], v[198:201], v[224:227], v[18:21]
	v_mfma_f32_16x16x32_bf16 v[6:9], v[190:193], v[232:235], v[6:9]
	v_mfma_f32_16x16x32_bf16 v[2:5], v[198:201], v[232:235], v[2:5]
	v_mfma_f32_16x16x32_bf16 v[54:57], v[194:197], v[212:215], v[54:57]
	v_mfma_f32_16x16x32_bf16 v[50:53], v[202:205], v[212:215], v[50:53]
	v_mfma_f32_16x16x32_bf16 v[38:41], v[194:197], v[220:223], v[38:41]
	v_mfma_f32_16x16x32_bf16 v[34:37], v[202:205], v[220:223], v[34:37]
	v_mfma_f32_16x16x32_bf16 v[22:25], v[194:197], v[228:231], v[22:25]
	v_mfma_f32_16x16x32_bf16 v[18:21], v[202:205], v[228:231], v[18:21]
	v_mfma_f32_16x16x32_bf16 v[6:9], v[194:197], v[236:239], v[6:9]
	v_mfma_f32_16x16x32_bf16 v[2:5], v[202:205], v[236:239], v[2:5]
	s_barrier
	s_setprio 0
	s_add_u32 s40, s40, 0x100
	s_addc_u32 s41, s41, 0
	s_cmp_ge_i32 s75, s54
	s_cbranch_scc0 .LBB0_982

; #define PG8_STAGE(bufoff, gbase, voff) do { _Pragma("unroll") for (int _i = 0; _i < 2; ++_i) \
;         __builtin_amdgcn_global_load_lds((const unsigned*)((const char*)(gbase) + (voff)[_i]), (PG8_LAS unsigned*)(lds + (bufoff) + ldsw + _i * 8192), 16, 0, 0); } while (0)
; #define PG8_LDA(dst, b, h) do { _Pragma("unroll") for (int m = 0; m < 4; ++m) { const bf16x8 f0_ = *(const PG8_LAS bf16x8*)(lds + PG8_SA(b, h) + aoff + m * 2048), f1_ = *(const PG8_LAS bf16x8*)(lds + PG8_SA(b, h) + aoff + m * 2048 + 1024); dst[m].set(f0_, f1_); } } while (0)
; #define PG8_LDB(dst, b, h) do { _Pragma("unroll") for (int n = 0; n < 2; ++n) { const bf16x8 f0_ = *(const PG8_LAS bf16x8*)(lds + PG8_SB(b, h) + boff + n * 2048), f1_ = *(const PG8_LAS bf16x8*)(lds + PG8_SB(b, h) + boff + n * 2048 + 1024); dst[n].set(f0_, f1_); } } while (0)
; #define PG8_WAIT_V(n) asm volatile("s_waitcnt vmcnt(" #n ")" ::: "memory")
; #define PG8_WAIT_L(n) asm volatile("s_waitcnt lgkmcnt(" #n ")" ::: "memory")
; #define PG8_BAR __builtin_amdgcn_s_barrier()
; #define PG8_SCHED __builtin_amdgcn_sched_barrier(0)
; template <class Epi, class Sched, bool ALIGN_EPI = false, bool SP2 = false>
; __device__ __forceinline__ void gemm_phase(PG8_LAS unsigned char* lds, const Gemm g, const Sched& S, const Epi& E) {
;     ...
;             PG8_LDB(B0, 0, 0); PG8_LDB(B1, 0, 1); PG8_SCHED; PG8_LDA(At, 0, 0); PG8_STAGE(PG8_SA(1, 1), a1 + hstep, voffA);
;             PG8_WAIT_V(8); PG8_WAIT_L(0); PG8_BAR; PG8_MMA(0, 0, At, B0); PG8_MMA(0, 1, At, B1); PG8_BAR; PG8_SCHED;
;             PG8_LDA(At, 0, 1); PG8_STAGE(PG8_SB(0, 0), b2, voffB); PG8_STAGE(PG8_SB(0, 1), b2 + hstepB, voffB); PG8_STAGE(PG8_SA(0, 0), a2, voffA);
;             PG8_WAIT_V(8); PG8_WAIT_L(0); PG8_BAR; PG8_MMA(1, 0, At, B0); PG8_MMA(1, 1, At, B1); PG8_BAR; PG8_SCHED;
.Lkr2_a:
	v_lshl_add_u64 v[224:225], s[56:57], 0, v[176:177]
	s_add_i32 m0, s67, 0xc000
	ds_read_b128 v[162:165], v195
	ds_read_b128 v[186:189], v195 offset:1024
	ds_read_b128 v[198:201], v195 offset:2048
	ds_read_b128 v[202:205], v195 offset:3072
	ds_read_b128 v[206:209], v195 offset:4096
	ds_read_b128 v[212:215], v195 offset:5120
	ds_read_b128 v[216:219], v195 offset:6144
	ds_read_b128 v[220:223], v195 offset:7168
	global_load_lds_dwordx4 v[224:225], off
	v_lshl_add_u64 v[224:225], s[56:57], 0, v[178:179]
	s_add_i32 m0, s67, 0xe000
	s_nop 0
	global_load_lds_dwordx4 v[224:225], off
	s_waitcnt vmcnt(8)
	s_waitcnt lgkmcnt(0)
	s_barrier
	s_setprio 1
	s_waitcnt lgkmcnt(0)
	v_mfma_f32_16x16x32_bf16 v[126:129], v[130:133], v[162:165], v[126:129]
	v_mfma_f32_16x16x32_bf16 v[122:125], v[138:141], v[162:165], v[122:125]
	v_mfma_f32_16x16x32_bf16 v[58:61], v[130:133], v[198:201], v[58:61]
	v_mfma_f32_16x16x32_bf16 v[62:65], v[138:141], v[198:201], v[62:65]
	v_mfma_f32_16x16x32_bf16 v[106:109], v[130:133], v[206:209], v[106:109]
	v_mfma_f32_16x16x32_bf16 v[110:113], v[138:141], v[206:209], v[110:113]
	v_mfma_f32_16x16x32_bf16 v[98:101], v[130:133], v[216:219], v[98:101]
	v_mfma_f32_16x16x32_bf16 v[102:105], v[138:141], v[216:219], v[102:105]
	v_mfma_f32_16x16x32_bf16 v[126:129], v[134:137], v[186:189], v[126:129]
	v_mfma_f32_16x16x32_bf16 v[122:125], v[142:145], v[186:189], v[122:125]
	v_mfma_f32_16x16x32_bf16 v[58:61], v[134:137], v[202:205], v[58:61]
	v_mfma_f32_16x16x32_bf16 v[62:65], v[142:145], v[202:205], v[62:65]
	v_mfma_f32_16x16x32_bf16 v[106:109], v[134:137], v[212:215], v[106:109]
	v_mfma_f32_16x16x32_bf16 v[110:113], v[142:145], v[212:215], v[110:113]
	v_mfma_f32_16x16x32_bf16 v[98:101], v[134:137], v[220:223], v[98:101]
	v_mfma_f32_16x16x32_bf16 v[102:105], v[142:145], v[220:223], v[102:105]
	v_mfma_f32_16x16x32_bf16 v[118:121], v[146:149], v[162:165], v[118:121]
	v_mfma_f32_16x16x32_bf16 v[114:117], v[154:157], v[162:165], v[114:117]
	v_mfma_f32_16x16x32_bf16 v[50:53], v[146:149], v[198:201], v[50:53]
	v_mfma_f32_16x16x32_bf16 v[54:57], v[154:157], v[198:201], v[54:57]
	v_mfma_f32_16x16x32_bf16 v[90:93], v[146:149], v[206:209], v[90:93]
	v_mfma_f32_16x16x32_bf16 v[94:97], v[154:157], v[206:209], v[94:97]
	v_mfma_f32_16x16x32_bf16 v[74:77], v[146:149], v[216:219], v[74:77]
	v_mfma_f32_16x16x32_bf16 v[78:81], v[154:157], v[216:219], v[78:81]
	v_mfma_f32_16x16x32_bf16 v[118:121], v[150:153], v[186:189], v[118:121]
	v_mfma_f32_16x16x32_bf16 v[114:117], v[158:161], v[186:189], v[114:117]
	v_mfma_f32_16x16x32_bf16 v[50:53], v[150:153], v[202:205], v[50:53]
	v_mfma_f32_16x16x32_bf16 v[54:57], v[158:161], v[202:205], v[54:57]
	v_mfma_f32_16x16x32_bf16 v[90:93], v[150:153], v[212:215], v[90:93]
	v_mfma_f32_16x16x32_bf16 v[94:97], v[158:161], v[212:215], v[94:97]
	v_mfma_f32_16x16x32_bf16 v[74:77], v[150:153], v[220:223], v[74:77]
	v_mfma_f32_16x16x32_bf16 v[78:81], v[158:161], v[220:223], v[78:81]
	s_barrier
	s_setprio 0
	s_add_i32 s33, s82, s66
	v_lshl_add_u64 v[224:225], s[0:1], 0, v[168:169]
	s_mov_b32 m0, s33
	ds_read_b128 v[162:165], v195 offset:16384
	ds_read_b128 v[186:189], v195 offset:17408
	ds_read_b128 v[198:201], v195 offset:18432
	ds_read_b128 v[202:205], v195 offset:19456
	ds_read_b128 v[206:209], v195 offset:20480
	ds_read_b128 v[212:215], v195 offset:21504
	ds_read_b128 v[216:219], v195 offset:22528
	ds_read_b128 v[220:223], v195 offset:23552
	global_load_lds_dwordx4 v[224:225], off
	s_add_i32 m0, s33, 0x2000
	v_lshl_add_u64 v[226:227], s[0:1], 0, v[172:173]
	s_add_u32 s0, s0, s16
	s_addc_u32 s1, s1, s17
	s_add_i32 s33, s83, s66
	global_load_lds_dwordx4 v[226:227], off
	v_lshl_add_u64 v[228:229], s[0:1], 0, v[168:169]
	s_mov_b32 m0, s33
	v_lshl_add_u64 v[230:231], s[0:1], 0, v[172:173]
	global_load_lds_dwordx4 v[228:229], off
	s_add_i32 m0, s33, 0x2000
	v_lshl_add_u64 v[232:233], s[58:59], 0, v[166:167]
	global_load_lds_dwordx4 v[230:231], off
	v_lshl_add_u64 v[234:235], s[58:59], 0, v[170:171]
	s_waitcnt vmcnt(6)
	s_waitcnt lgkmcnt(0)
	s_barrier
	s_setprio 1
	s_waitcnt lgkmcnt(0)
	v_mfma_f32_16x16x32_bf16 v[82:85], v[130:133], v[162:165], v[82:85]
	v_mfma_f32_16x16x32_bf16 v[86:89], v[138:141], v[162:165], v[86:89]
	v_mfma_f32_16x16x32_bf16 v[46:49], v[130:133], v[198:201], v[46:49]
	v_mfma_f32_16x16x32_bf16 v[42:45], v[138:141], v[198:201], v[42:45]
	v_mfma_f32_16x16x32_bf16 v[30:33], v[130:133], v[206:209], v[30:33]
	v_mfma_f32_16x16x32_bf16 v[26:29], v[138:141], v[206:209], v[26:29]
	v_mfma_f32_16x16x32_bf16 v[14:17], v[130:133], v[216:219], v[14:17]
	v_mfma_f32_16x16x32_bf16 v[6:9], v[138:141], v[216:219], v[6:9]
	v_mfma_f32_16x16x32_bf16 v[82:85], v[134:137], v[186:189], v[82:85]
	v_mfma_f32_16x16x32_bf16 v[86:89], v[142:145], v[186:189], v[86:89]
	v_mfma_f32_16x16x32_bf16 v[46:49], v[134:137], v[202:205], v[46:49]
	v_mfma_f32_16x16x32_bf16 v[42:45], v[142:145], v[202:205], v[42:45]
	v_mfma_f32_16x16x32_bf16 v[30:33], v[134:137], v[212:215], v[30:33]
	v_mfma_f32_16x16x32_bf16 v[26:29], v[142:145], v[212:215], v[26:29]
	v_mfma_f32_16x16x32_bf16 v[14:17], v[134:137], v[220:223], v[14:17]
	v_mfma_f32_16x16x32_bf16 v[6:9], v[142:145], v[220:223], v[6:9]
	v_mfma_f32_16x16x32_bf16 v[66:69], v[146:149], v[162:165], v[66:69]
	v_mfma_f32_16x16x32_bf16 v[70:73], v[154:157], v[162:165], v[70:73]
	v_mfma_f32_16x16x32_bf16 v[38:41], v[146:149], v[198:201], v[38:41]
	v_mfma_f32_16x16x32_bf16 v[34:37], v[154:157], v[198:201], v[34:37]
	v_mfma_f32_16x16x32_bf16 v[22:25], v[146:149], v[206:209], v[22:25]
	v_mfma_f32_16x16x32_bf16 v[18:21], v[154:157], v[206:209], v[18:21]
	v_mfma_f32_16x16x32_bf16 v[10:13], v[146:149], v[216:219], v[10:13]
	v_mfma_f32_16x16x32_bf16 v[2:5], v[154:157], v[216:219], v[2:5]
	v_mfma_f32_16x16x32_bf16 v[66:69], v[150:153], v[186:189], v[66:69]
	v_mfma_f32_16x16x32_bf16 v[70:73], v[158:161], v[186:189], v[70:73]
	v_mfma_f32_16x16x32_bf16 v[38:41], v[150:153], v[202:205], v[38:41]
	v_mfma_f32_16x16x32_bf16 v[34:37], v[158:161], v[202:205], v[34:37]
	v_mfma_f32_16x16x32_bf16 v[22:25], v[150:153], v[212:215], v[22:25]
	v_mfma_f32_16x16x32_bf16 v[18:21], v[158:161], v[212:215], v[18:21]
	v_mfma_f32_16x16x32_bf16 v[10:13], v[150:153], v[220:223], v[10:13]
	v_mfma_f32_16x16x32_bf16 v[2:5], v[158:161], v[220:223], v[2:5]
	s_barrier
; #define PG8_STAGE(bufoff, gbase, voff) do { _Pragma("unroll") for (int _i = 0; _i < 2; ++_i) \
;         __builtin_amdgcn_global_load_lds((const unsigned*)((const char*)(gbase) + (voff)[_i]), (PG8_LAS unsigned*)(lds + (bufoff) + ldsw + _i * 8192), 16, 0, 0); } while (0)
; #define PG8_LDA(dst, b, h) do { _Pragma("unroll") for (int m = 0; m < 4; ++m) { const bf16x8 f0_ = *(const PG8_LAS bf16x8*)(lds + PG8_SA(b, h) + aoff + m * 2048), f1_ = *(const PG8_LAS bf16x8*)(lds + PG8_SA(b, h) + aoff + m * 2048 + 1024); dst[m].set(f0_, f1_); } } while (0)
; #define PG8_LDB(dst, b, h) do { _Pragma("unroll") for (int n = 0; n < 2; ++n) { const bf16x8 f0_ = *(const PG8_LAS bf16x8*)(lds + PG8_SB(b, h) + boff + n * 2048), f1_ = *(const PG8_LAS bf16x8*)(lds + PG8_SB(b, h) + boff + n * 2048 + 1024); dst[n].set(f0_, f1_); } } while (0)
; #define PG8_WAIT_V(n) asm volatile("s_waitcnt vmcnt(" #n ")" ::: "memory")
; #define PG8_WAIT_L(n) asm volatile("s_waitcnt lgkmcnt(" #n ")" ::: "memory")
; #define PG8_BAR __builtin_amdgcn_s_barrier()
; #define PG8_SCHED __builtin_amdgcn_sched_barrier(0)
; template <class Epi, class Sched, bool ALIGN_EPI = false, bool SP2 = false>
; __device__ __forceinline__ void gemm_phase(PG8_LAS unsigned char* lds, const Gemm g, const Sched& S, const Epi& E) {
;     ...
;             PG8_LDB(B0, 1, 0); PG8_LDB(B1, 1, 1); PG8_SCHED; PG8_LDA(At, 1, 0); PG8_STAGE(PG8_SA(0, 1), a2 + hstep, voffA);
;             PG8_WAIT_V(8); PG8_WAIT_L(0); PG8_BAR; PG8_MMA(0, 0, At, B0); PG8_MMA(0, 1, At, B1); PG8_BAR; PG8_SCHED;
;             PG8_LDA(At, 1, 1); PG8_STAGE(PG8_SB(1, 0), b3, voffB); PG8_STAGE(PG8_SB(1, 1), b3 + hstepB, voffB); PG8_STAGE(PG8_SA(1, 0), a3, voffA);
;             PG8_WAIT_V(8); PG8_WAIT_L(0); PG8_BAR; PG8_MMA(1, 0, At, B0); PG8_MMA(1, 1, At, B1); PG8_BAR; PG8_SCHED;
	s_setprio 0
	s_add_i32 s33, 0, 0x18000
	s_add_i32 s96, 0, 0x1c000
	v_add_u32_e32 v142, s33, v190
	v_add_u32_e32 v158, s96, v190
	ds_read_b128 v[130:133], v142
	ds_read_b128 v[134:137], v142 offset:1024
	ds_read_b128 v[138:141], v142 offset:2048
	ds_read_b128 v[142:145], v142 offset:3072
	ds_read_b128 v[146:149], v158
	ds_read_b128 v[150:153], v158 offset:1024
	ds_read_b128 v[154:157], v158 offset:2048
	ds_read_b128 v[158:161], v158 offset:3072
	s_add_u32 s0, s58, s14
	s_addc_u32 s1, s59, s15
	s_mov_b32 m0, s71
	v_lshl_add_u64 v[236:237], s[0:1], 0, v[166:167]
	ds_read_b128 v[162:165], v195 offset:32768
	ds_read_b128 v[186:189], v195 offset:33792
	ds_read_b128 v[198:201], v195 offset:34816
	ds_read_b128 v[202:205], v195 offset:35840
	ds_read_b128 v[206:209], v195 offset:36864
	ds_read_b128 v[212:215], v195 offset:37888
	ds_read_b128 v[216:219], v195 offset:38912
	ds_read_b128 v[220:223], v195 offset:39936
	s_mov_b32 m0, s67
	s_nop 0
	global_load_lds_dwordx4 v[232:233], off
	s_mov_b32 m0, s69
	s_nop 0
	global_load_lds_dwordx4 v[234:235], off
	s_mov_b32 m0, s71
	s_nop 0
	global_load_lds_dwordx4 v[236:237], off
	v_lshl_add_u64 v[236:237], s[0:1], 0, v[170:171]
	s_mov_b32 m0, s73
	s_nop 0
	global_load_lds_dwordx4 v[236:237], off
	s_waitcnt vmcnt(8)
	s_waitcnt lgkmcnt(0)
	s_barrier
	s_setprio 1
	s_waitcnt lgkmcnt(0)
	v_mfma_f32_16x16x32_bf16 v[126:129], v[130:133], v[162:165], v[126:129]
	v_mfma_f32_16x16x32_bf16 v[122:125], v[138:141], v[162:165], v[122:125]
	v_mfma_f32_16x16x32_bf16 v[58:61], v[130:133], v[198:201], v[58:61]
	v_mfma_f32_16x16x32_bf16 v[62:65], v[138:141], v[198:201], v[62:65]
	v_mfma_f32_16x16x32_bf16 v[106:109], v[130:133], v[206:209], v[106:109]
	v_mfma_f32_16x16x32_bf16 v[110:113], v[138:141], v[206:209], v[110:113]
	v_mfma_f32_16x16x32_bf16 v[98:101], v[130:133], v[216:219], v[98:101]
	v_mfma_f32_16x16x32_bf16 v[102:105], v[138:141], v[216:219], v[102:105]
	v_mfma_f32_16x16x32_bf16 v[126:129], v[134:137], v[186:189], v[126:129]
	v_mfma_f32_16x16x32_bf16 v[122:125], v[142:145], v[186:189], v[122:125]
	v_mfma_f32_16x16x32_bf16 v[58:61], v[134:137], v[202:205], v[58:61]
	v_mfma_f32_16x16x32_bf16 v[62:65], v[142:145], v[202:205], v[62:65]
	v_mfma_f32_16x16x32_bf16 v[106:109], v[134:137], v[212:215], v[106:109]
	v_mfma_f32_16x16x32_bf16 v[110:113], v[142:145], v[212:215], v[110:113]
	v_mfma_f32_16x16x32_bf16 v[98:101], v[134:137], v[220:223], v[98:101]
	v_mfma_f32_16x16x32_bf16 v[102:105], v[142:145], v[220:223], v[102:105]
	v_mfma_f32_16x16x32_bf16 v[118:121], v[146:149], v[162:165], v[118:121]
	v_mfma_f32_16x16x32_bf16 v[114:117], v[154:157], v[162:165], v[114:117]
	v_mfma_f32_16x16x32_bf16 v[50:53], v[146:149], v[198:201], v[50:53]
	v_mfma_f32_16x16x32_bf16 v[54:57], v[154:157], v[198:201], v[54:57]
	v_mfma_f32_16x16x32_bf16 v[90:93], v[146:149], v[206:209], v[90:93]
	v_mfma_f32_16x16x32_bf16 v[94:97], v[154:157], v[206:209], v[94:97]
	v_mfma_f32_16x16x32_bf16 v[74:77], v[146:149], v[216:219], v[74:77]
	v_mfma_f32_16x16x32_bf16 v[78:81], v[154:157], v[216:219], v[78:81]
	v_mfma_f32_16x16x32_bf16 v[118:121], v[150:153], v[186:189], v[118:121]
	v_mfma_f32_16x16x32_bf16 v[114:117], v[158:161], v[186:189], v[114:117]
	v_mfma_f32_16x16x32_bf16 v[50:53], v[150:153], v[202:205], v[50:53]
	v_mfma_f32_16x16x32_bf16 v[54:57], v[158:161], v[202:205], v[54:57]
	v_mfma_f32_16x16x32_bf16 v[90:93], v[150:153], v[212:215], v[90:93]
	v_mfma_f32_16x16x32_bf16 v[94:97], v[158:161], v[212:215], v[94:97]
	v_mfma_f32_16x16x32_bf16 v[74:77], v[150:153], v[220:223], v[74:77]
	v_mfma_f32_16x16x32_bf16 v[78:81], v[158:161], v[220:223], v[78:81]
	s_barrier
	s_setprio 0
	s_add_i32 s0, s33, s66
	v_lshl_add_u64 v[224:225], v[224:225], 0, s[28:29]
	s_mov_b32 m0, s0
	ds_read_b128 v[162:165], v195 offset:49152
	ds_read_b128 v[186:189], v195 offset:50176
	ds_read_b128 v[198:201], v195 offset:51200
	ds_read_b128 v[202:205], v195 offset:52224
	ds_read_b128 v[206:209], v195 offset:53248
	ds_read_b128 v[212:215], v195 offset:54272
	ds_read_b128 v[216:219], v195 offset:55296
	ds_read_b128 v[220:223], v195 offset:56320
	global_load_lds_dwordx4 v[224:225], off
	v_lshl_add_u64 v[224:225], v[226:227], 0, s[28:29]
	s_add_i32 m0, s0, 0x2000
	s_add_i32 s0, s96, s66
	global_load_lds_dwordx4 v[224:225], off
	v_lshl_add_u64 v[224:225], v[228:229], 0, s[28:29]
	s_mov_b32 m0, s0
	s_nop 0
	global_load_lds_dwordx4 v[224:225], off
	v_lshl_add_u64 v[224:225], v[230:231], 0, s[28:29]
	s_add_i32 m0, s0, 0x2000
	s_nop 0
	global_load_lds_dwordx4 v[224:225], off
	s_cmp_ge_i32 s95, s76
	s_cbranch_scc0 .Lkr2_b
	v_lshl_add_u64 v[224:225], v[232:233], 0, s[28:29]
	s_mov_b32 m0, s74
	s_nop 0
	global_load_lds_dwordx4 v[224:225], off
	v_lshl_add_u64 v[224:225], v[234:235], 0, s[28:29]
	s_mov_b32 m0, s75
	s_nop 0
	global_load_lds_dwordx4 v[224:225], off
; #define PG8_STAGE(bufoff, gbase, voff) do { _Pragma("unroll") for (int _i = 0; _i < 2; ++_i) \
;         __builtin_amdgcn_global_load_lds((const unsigned*)((const char*)(gbase) + (voff)[_i]), (PG8_LAS unsigned*)(lds + (bufoff) + ldsw + _i * 8192), 16, 0, 0); } while (0)
; #define PG8_LDA(dst, b, h) do { _Pragma("unroll") for (int m = 0; m < 4; ++m) { const bf16x8 f0_ = *(const PG8_LAS bf16x8*)(lds + PG8_SA(b, h) + aoff + m * 2048), f1_ = *(const PG8_LAS bf16x8*)(lds + PG8_SA(b, h) + aoff + m * 2048 + 1024); dst[m].set(f0_, f1_); } } while (0)
; #define PG8_WAIT_V(n) asm volatile("s_waitcnt vmcnt(" #n ")" ::: "memory")
; #define PG8_WAIT_L(n) asm volatile("s_waitcnt lgkmcnt(" #n ")" ::: "memory")
; #define PG8_BAR __builtin_amdgcn_s_barrier()
; #define PG8_SCHED __builtin_amdgcn_sched_barrier(0)
; template <class Epi, class Sched, bool ALIGN_EPI = false, bool SP2 = false>
; __device__ __forceinline__ void gemm_phase(PG8_LAS unsigned char* lds, const Gemm g, const Sched& S, const Epi& E) {
;     ...
;         for (int t = 0; t < nt; t += 2) {
;             if constexpr (Epi::MIDK) { if (t == (nt >> 1)) E.mid(acc, cur, wr, wc, fr, fq); }
;             const bool last = (t == nt - 2);
;             const char* a1 = cA + (size_t)(t + 1) * kstep;
;             const char* a2 = last ? nA : cA + (size_t)(t + 2) * kstep; const char* b2 = last ? nB : cB + (size_t)(t + 2) * kstep;
;     ...
;             PG8_LDA(At, 1, 1); PG8_STAGE(PG8_SB(1, 0), b3, voffB); PG8_STAGE(PG8_SB(1, 1), b3 + hstepB, voffB); PG8_STAGE(PG8_SA(1, 0), a3, voffA);
;             PG8_WAIT_V(8); PG8_WAIT_L(0); PG8_BAR; PG8_MMA(1, 0, At, B0); PG8_MMA(1, 1, At, B1); PG8_BAR; PG8_SCHED;
.Lkr2_b:
	s_waitcnt vmcnt(6)
	s_waitcnt lgkmcnt(0)
	s_barrier
	s_setprio 1
	s_waitcnt lgkmcnt(0)
	v_mfma_f32_16x16x32_bf16 v[82:85], v[130:133], v[162:165], v[82:85]
	v_mfma_f32_16x16x32_bf16 v[86:89], v[138:141], v[162:165], v[86:89]
	v_mfma_f32_16x16x32_bf16 v[46:49], v[130:133], v[198:201], v[46:49]
	v_mfma_f32_16x16x32_bf16 v[42:45], v[138:141], v[198:201], v[42:45]
	v_mfma_f32_16x16x32_bf16 v[30:33], v[130:133], v[206:209], v[30:33]
	v_mfma_f32_16x16x32_bf16 v[26:29], v[138:141], v[206:209], v[26:29]
	v_mfma_f32_16x16x32_bf16 v[14:17], v[130:133], v[216:219], v[14:17]
	v_mfma_f32_16x16x32_bf16 v[6:9], v[138:141], v[216:219], v[6:9]
	v_mfma_f32_16x16x32_bf16 v[82:85], v[134:137], v[186:189], v[82:85]
	v_mfma_f32_16x16x32_bf16 v[86:89], v[142:145], v[186:189], v[86:89]
	v_mfma_f32_16x16x32_bf16 v[46:49], v[134:137], v[202:205], v[46:49]
	v_mfma_f32_16x16x32_bf16 v[42:45], v[142:145], v[202:205], v[42:45]
	v_mfma_f32_16x16x32_bf16 v[30:33], v[134:137], v[212:215], v[30:33]
	v_mfma_f32_16x16x32_bf16 v[26:29], v[142:145], v[212:215], v[26:29]
	v_mfma_f32_16x16x32_bf16 v[14:17], v[134:137], v[220:223], v[14:17]
	v_mfma_f32_16x16x32_bf16 v[6:9], v[142:145], v[220:223], v[6:9]
	v_mfma_f32_16x16x32_bf16 v[66:69], v[146:149], v[162:165], v[66:69]
	v_mfma_f32_16x16x32_bf16 v[70:73], v[154:157], v[162:165], v[70:73]
	v_mfma_f32_16x16x32_bf16 v[38:41], v[146:149], v[198:201], v[38:41]
	v_mfma_f32_16x16x32_bf16 v[34:37], v[154:157], v[198:201], v[34:37]
	v_mfma_f32_16x16x32_bf16 v[22:25], v[146:149], v[206:209], v[22:25]
	v_mfma_f32_16x16x32_bf16 v[18:21], v[154:157], v[206:209], v[18:21]
	v_mfma_f32_16x16x32_bf16 v[10:13], v[146:149], v[216:219], v[10:13]
	v_mfma_f32_16x16x32_bf16 v[2:5], v[154:157], v[216:219], v[2:5]
	v_mfma_f32_16x16x32_bf16 v[66:69], v[150:153], v[186:189], v[66:69]
	v_mfma_f32_16x16x32_bf16 v[70:73], v[158:161], v[186:189], v[70:73]
	v_mfma_f32_16x16x32_bf16 v[38:41], v[150:153], v[202:205], v[38:41]
	v_mfma_f32_16x16x32_bf16 v[34:37], v[158:161], v[202:205], v[34:37]
	v_mfma_f32_16x16x32_bf16 v[22:25], v[150:153], v[212:215], v[22:25]
	v_mfma_f32_16x16x32_bf16 v[18:21], v[158:161], v[212:215], v[18:21]
	v_mfma_f32_16x16x32_bf16 v[10:13], v[150:153], v[220:223], v[10:13]
	v_mfma_f32_16x16x32_bf16 v[2:5], v[158:161], v[220:223], v[2:5]
	s_barrier
	s_setprio 0
	s_add_u32 s56, s56, 0x100
	s_addc_u32 s57, s57, 0
	s_add_u32 s93, s93, 0x100
	s_addc_u32 s94, s94, 0
	s_cmp_ge_i32 s95, s76
	s_cselect_b32 s99, 0, 1
	s_mov_b32 s58, s95
	s_cbranch_scc0 .LBB0_1070
	v_readlane_b32 s94, v254, 5
	v_readlane_b32 s95, v254, 6

; #define PG8_STAGE(bufoff, gbase, voff) do { _Pragma("unroll") for (int _i = 0; _i < 2; ++_i) \
;         __builtin_amdgcn_global_load_lds((const unsigned*)((const char*)(gbase) + (voff)[_i]), (PG8_LAS unsigned*)(lds + (bufoff) + ldsw + _i * 8192), 16, 0, 0); } while (0)
; #define PG8_LDA(dst, b, h) do { _Pragma("unroll") for (int m = 0; m < 4; ++m) { const bf16x8 f0_ = *(const PG8_LAS bf16x8*)(lds + PG8_SA(b, h) + aoff + m * 2048), f1_ = *(const PG8_LAS bf16x8*)(lds + PG8_SA(b, h) + aoff + m * 2048 + 1024); dst[m].set(f0_, f1_); } } while (0)
; #define PG8_LDB(dst, b, h) do { _Pragma("unroll") for (int n = 0; n < 2; ++n) { const bf16x8 f0_ = *(const PG8_LAS bf16x8*)(lds + PG8_SB(b, h) + boff + n * 2048), f1_ = *(const PG8_LAS bf16x8*)(lds + PG8_SB(b, h) + boff + n * 2048 + 1024); dst[n].set(f0_, f1_); } } while (0)
; #define PG8_WAIT_V(n) asm volatile("s_waitcnt vmcnt(" #n ")" ::: "memory")
; #define PG8_WAIT_L(n) asm volatile("s_waitcnt lgkmcnt(" #n ")" ::: "memory")
; #define PG8_BAR __builtin_amdgcn_s_barrier()
; #define PG8_SCHED __builtin_amdgcn_sched_barrier(0)
; template <class Epi, class Sched, bool ALIGN_EPI = false, bool SP2 = false>
; __device__ __forceinline__ void gemm_phase(PG8_LAS unsigned char* lds, const Gemm g, const Sched& S, const Epi& E) {
;     ...
;             PG8_LDB(B0, 0, 0); PG8_LDB(B1, 0, 1); PG8_SCHED; PG8_LDA(At, 0, 0); PG8_STAGE(PG8_SA(1, 1), a1 + hstep, voffA);
;             PG8_WAIT_V(8); PG8_WAIT_L(0); PG8_BAR; PG8_MMA(0, 0, At, B0); PG8_MMA(0, 1, At, B1); PG8_BAR; PG8_SCHED;
;             PG8_LDA(At, 0, 1); PG8_STAGE(PG8_SB(0, 0), b2, voffB); PG8_STAGE(PG8_SB(0, 1), b2 + hstepB, voffB); PG8_STAGE(PG8_SA(0, 0), a2, voffA);
;             PG8_WAIT_V(8); PG8_WAIT_L(0); PG8_BAR; PG8_MMA(1, 0, At, B0); PG8_MMA(1, 1, At, B1); PG8_BAR; PG8_SCHED;
.Lkr3_a:
	v_lshl_add_u64 v[148:149], s[30:31], 0, v[140:141]
	s_add_i32 m0, s40, 0xc000
	ds_read_b128 v[188:191], v154
	ds_read_b128 v[192:195], v154 offset:1024
	ds_read_b128 v[196:199], v154 offset:2048
	ds_read_b128 v[200:203], v154 offset:3072
	ds_read_b128 v[204:207], v154 offset:4096
	ds_read_b128 v[212:215], v154 offset:5120
	ds_read_b128 v[216:219], v154 offset:6144
	ds_read_b128 v[220:223], v154 offset:7168
	global_load_lds_dwordx4 v[148:149], off
	v_lshl_add_u64 v[148:149], s[30:31], 0, v[142:143]
	s_add_i32 m0, s40, 0xe000
	s_nop 0
	global_load_lds_dwordx4 v[148:149], off
	s_waitcnt vmcnt(8)
	s_waitcnt lgkmcnt(0)
	s_barrier
	s_setprio 1
	s_waitcnt lgkmcnt(0)
	v_mfma_f32_16x16x32_bf16 v[126:129], v[156:159], v[188:191], v[126:129]
	v_mfma_f32_16x16x32_bf16 v[122:125], v[164:167], v[188:191], v[122:125]
	v_mfma_f32_16x16x32_bf16 v[110:113], v[156:159], v[196:199], v[110:113]
	v_mfma_f32_16x16x32_bf16 v[106:109], v[164:167], v[196:199], v[106:109]
	v_mfma_f32_16x16x32_bf16 v[94:97], v[156:159], v[204:207], v[94:97]
	v_mfma_f32_16x16x32_bf16 v[90:93], v[164:167], v[204:207], v[90:93]
	v_mfma_f32_16x16x32_bf16 v[78:81], v[156:159], v[216:219], v[78:81]
	v_mfma_f32_16x16x32_bf16 v[74:77], v[164:167], v[216:219], v[74:77]
	v_mfma_f32_16x16x32_bf16 v[126:129], v[160:163], v[192:195], v[126:129]
	v_mfma_f32_16x16x32_bf16 v[122:125], v[168:171], v[192:195], v[122:125]
	v_mfma_f32_16x16x32_bf16 v[110:113], v[160:163], v[200:203], v[110:113]
	v_mfma_f32_16x16x32_bf16 v[106:109], v[168:171], v[200:203], v[106:109]
	v_mfma_f32_16x16x32_bf16 v[94:97], v[160:163], v[212:215], v[94:97]
	v_mfma_f32_16x16x32_bf16 v[90:93], v[168:171], v[212:215], v[90:93]
	v_mfma_f32_16x16x32_bf16 v[78:81], v[160:163], v[220:223], v[78:81]
	v_mfma_f32_16x16x32_bf16 v[74:77], v[168:171], v[220:223], v[74:77]
	v_mfma_f32_16x16x32_bf16 v[118:121], v[172:175], v[188:191], v[118:121]
	v_mfma_f32_16x16x32_bf16 v[114:117], v[180:183], v[188:191], v[114:117]
	v_mfma_f32_16x16x32_bf16 v[102:105], v[172:175], v[196:199], v[102:105]
	v_mfma_f32_16x16x32_bf16 v[98:101], v[180:183], v[196:199], v[98:101]
	v_mfma_f32_16x16x32_bf16 v[86:89], v[172:175], v[204:207], v[86:89]
	v_mfma_f32_16x16x32_bf16 v[82:85], v[180:183], v[204:207], v[82:85]
	v_mfma_f32_16x16x32_bf16 v[70:73], v[172:175], v[216:219], v[70:73]
	v_mfma_f32_16x16x32_bf16 v[66:69], v[180:183], v[216:219], v[66:69]
	v_mfma_f32_16x16x32_bf16 v[118:121], v[176:179], v[192:195], v[118:121]
	v_mfma_f32_16x16x32_bf16 v[114:117], v[184:187], v[192:195], v[114:117]
	v_mfma_f32_16x16x32_bf16 v[102:105], v[176:179], v[200:203], v[102:105]
	v_mfma_f32_16x16x32_bf16 v[98:101], v[184:187], v[200:203], v[98:101]
	v_mfma_f32_16x16x32_bf16 v[86:89], v[176:179], v[212:215], v[86:89]
	v_mfma_f32_16x16x32_bf16 v[82:85], v[184:187], v[212:215], v[82:85]
	v_mfma_f32_16x16x32_bf16 v[70:73], v[176:179], v[220:223], v[70:73]
	v_mfma_f32_16x16x32_bf16 v[66:69], v[184:187], v[220:223], v[66:69]
	s_barrier
	s_setprio 0
	s_add_i32 s33, s52, s39
	v_lshl_add_u64 v[148:149], s[0:1], 0, v[132:133]
	s_mov_b32 m0, s33
	ds_read_b128 v[188:191], v154 offset:16384
	ds_read_b128 v[192:195], v154 offset:17408
	ds_read_b128 v[196:199], v154 offset:18432
	ds_read_b128 v[200:203], v154 offset:19456
	ds_read_b128 v[204:207], v154 offset:20480
	ds_read_b128 v[212:215], v154 offset:21504
	ds_read_b128 v[216:219], v154 offset:22528
	ds_read_b128 v[220:223], v154 offset:23552
	global_load_lds_dwordx4 v[148:149], off
	s_add_i32 m0, s33, 0x2000
	v_lshl_add_u64 v[208:209], s[0:1], 0, v[136:137]
	s_add_u32 s0, s0, s14
	s_addc_u32 s1, s1, s15
	s_add_i32 s33, s53, s39
	global_load_lds_dwordx4 v[208:209], off
	v_lshl_add_u64 v[224:225], s[0:1], 0, v[132:133]
	s_mov_b32 m0, s33
	v_lshl_add_u64 v[226:227], s[0:1], 0, v[136:137]
	global_load_lds_dwordx4 v[224:225], off
	s_add_i32 m0, s33, 0x2000
	v_lshl_add_u64 v[228:229], s[34:35], 0, v[130:131]
	global_load_lds_dwordx4 v[226:227], off
	v_lshl_add_u64 v[230:231], s[34:35], 0, v[134:135]
	s_waitcnt vmcnt(6)
	s_waitcnt lgkmcnt(0)
	s_barrier
	s_setprio 1
	s_waitcnt lgkmcnt(0)
	v_mfma_f32_16x16x32_bf16 v[62:65], v[156:159], v[188:191], v[62:65]
	v_mfma_f32_16x16x32_bf16 v[58:61], v[164:167], v[188:191], v[58:61]
	v_mfma_f32_16x16x32_bf16 v[46:49], v[156:159], v[196:199], v[46:49]
	v_mfma_f32_16x16x32_bf16 v[42:45], v[164:167], v[196:199], v[42:45]
	v_mfma_f32_16x16x32_bf16 v[30:33], v[156:159], v[204:207], v[30:33]
	v_mfma_f32_16x16x32_bf16 v[26:29], v[164:167], v[204:207], v[26:29]
	v_mfma_f32_16x16x32_bf16 v[14:17], v[156:159], v[216:219], v[14:17]
	v_mfma_f32_16x16x32_bf16 v[6:9], v[164:167], v[216:219], v[6:9]
	v_mfma_f32_16x16x32_bf16 v[62:65], v[160:163], v[192:195], v[62:65]
	v_mfma_f32_16x16x32_bf16 v[58:61], v[168:171], v[192:195], v[58:61]
	v_mfma_f32_16x16x32_bf16 v[46:49], v[160:163], v[200:203], v[46:49]
	v_mfma_f32_16x16x32_bf16 v[42:45], v[168:171], v[200:203], v[42:45]
	v_mfma_f32_16x16x32_bf16 v[30:33], v[160:163], v[212:215], v[30:33]
	v_mfma_f32_16x16x32_bf16 v[26:29], v[168:171], v[212:215], v[26:29]
	v_mfma_f32_16x16x32_bf16 v[14:17], v[160:163], v[220:223], v[14:17]
	v_mfma_f32_16x16x32_bf16 v[6:9], v[168:171], v[220:223], v[6:9]
	v_mfma_f32_16x16x32_bf16 v[54:57], v[172:175], v[188:191], v[54:57]
	v_mfma_f32_16x16x32_bf16 v[50:53], v[180:183], v[188:191], v[50:53]
	v_mfma_f32_16x16x32_bf16 v[38:41], v[172:175], v[196:199], v[38:41]
	v_mfma_f32_16x16x32_bf16 v[34:37], v[180:183], v[196:199], v[34:37]
	v_mfma_f32_16x16x32_bf16 v[22:25], v[172:175], v[204:207], v[22:25]
	v_mfma_f32_16x16x32_bf16 v[18:21], v[180:183], v[204:207], v[18:21]
	v_mfma_f32_16x16x32_bf16 v[10:13], v[172:175], v[216:219], v[10:13]
	v_mfma_f32_16x16x32_bf16 v[2:5], v[180:183], v[216:219], v[2:5]
	v_mfma_f32_16x16x32_bf16 v[54:57], v[176:179], v[192:195], v[54:57]
	v_mfma_f32_16x16x32_bf16 v[50:53], v[184:187], v[192:195], v[50:53]
	v_mfma_f32_16x16x32_bf16 v[38:41], v[176:179], v[200:203], v[38:41]
	v_mfma_f32_16x16x32_bf16 v[34:37], v[184:187], v[200:203], v[34:37]
	v_mfma_f32_16x16x32_bf16 v[22:25], v[176:179], v[212:215], v[22:25]
	v_mfma_f32_16x16x32_bf16 v[18:21], v[184:187], v[212:215], v[18:21]
	v_mfma_f32_16x16x32_bf16 v[10:13], v[176:179], v[220:223], v[10:13]
	v_mfma_f32_16x16x32_bf16 v[2:5], v[184:187], v[220:223], v[2:5]
	s_barrier
; #define PG8_STAGE(bufoff, gbase, voff) do { _Pragma("unroll") for (int _i = 0; _i < 2; ++_i) \
;         __builtin_amdgcn_global_load_lds((const unsigned*)((const char*)(gbase) + (voff)[_i]), (PG8_LAS unsigned*)(lds + (bufoff) + ldsw + _i * 8192), 16, 0, 0); } while (0)
; #define PG8_LDA(dst, b, h) do { _Pragma("unroll") for (int m = 0; m < 4; ++m) { const bf16x8 f0_ = *(const PG8_LAS bf16x8*)(lds + PG8_SA(b, h) + aoff + m * 2048), f1_ = *(const PG8_LAS bf16x8*)(lds + PG8_SA(b, h) + aoff + m * 2048 + 1024); dst[m].set(f0_, f1_); } } while (0)
; #define PG8_LDB(dst, b, h) do { _Pragma("unroll") for (int n = 0; n < 2; ++n) { const bf16x8 f0_ = *(const PG8_LAS bf16x8*)(lds + PG8_SB(b, h) + boff + n * 2048), f1_ = *(const PG8_LAS bf16x8*)(lds + PG8_SB(b, h) + boff + n * 2048 + 1024); dst[n].set(f0_, f1_); } } while (0)
; #define PG8_WAIT_V(n) asm volatile("s_waitcnt vmcnt(" #n ")" ::: "memory")
; #define PG8_WAIT_L(n) asm volatile("s_waitcnt lgkmcnt(" #n ")" ::: "memory")
; #define PG8_BAR __builtin_amdgcn_s_barrier()
; #define PG8_SCHED __builtin_amdgcn_sched_barrier(0)
; template <class Epi, class Sched, bool ALIGN_EPI = false, bool SP2 = false>
; __device__ __forceinline__ void gemm_phase(PG8_LAS unsigned char* lds, const Gemm g, const Sched& S, const Epi& E) {
;     ...
;             PG8_LDB(B0, 1, 0); PG8_LDB(B1, 1, 1); PG8_SCHED; PG8_LDA(At, 1, 0); PG8_STAGE(PG8_SA(0, 1), a2 + hstep, voffA);
;             PG8_WAIT_V(8); PG8_WAIT_L(0); PG8_BAR; PG8_MMA(0, 0, At, B0); PG8_MMA(0, 1, At, B1); PG8_BAR; PG8_SCHED;
;             PG8_LDA(At, 1, 1); PG8_STAGE(PG8_SB(1, 0), b3, voffB); PG8_STAGE(PG8_SB(1, 1), b3 + hstepB, voffB); PG8_STAGE(PG8_SA(1, 0), a3, voffA);
;             PG8_WAIT_V(8); PG8_WAIT_L(0); PG8_BAR; PG8_MMA(1, 0, At, B0); PG8_MMA(1, 1, At, B1); PG8_BAR; PG8_SCHED;
	s_setprio 0
	s_add_i32 s33, 0, 0x18000
	s_add_i32 s63, 0, 0x1c000
	v_add_u32_e32 v168, s33, v1
	v_add_u32_e32 v184, s63, v1
	ds_read_b128 v[156:159], v168
	ds_read_b128 v[160:163], v168 offset:1024
	ds_read_b128 v[164:167], v168 offset:2048
	ds_read_b128 v[168:171], v168 offset:3072
	ds_read_b128 v[172:175], v184
	ds_read_b128 v[176:179], v184 offset:1024
	ds_read_b128 v[180:183], v184 offset:2048
	ds_read_b128 v[184:187], v184 offset:3072
	s_add_u32 s0, s34, s12
	s_addc_u32 s1, s35, s13
	s_mov_b32 m0, s42
	v_lshl_add_u64 v[232:233], s[0:1], 0, v[130:131]
	ds_read_b128 v[188:191], v154 offset:32768
	ds_read_b128 v[192:195], v154 offset:33792
	ds_read_b128 v[196:199], v154 offset:34816
	ds_read_b128 v[200:203], v154 offset:35840
	ds_read_b128 v[204:207], v154 offset:36864
	ds_read_b128 v[212:215], v154 offset:37888
	ds_read_b128 v[216:219], v154 offset:38912
	ds_read_b128 v[220:223], v154 offset:39936
	s_mov_b32 m0, s40
	s_nop 0
	global_load_lds_dwordx4 v[228:229], off
	s_mov_b32 m0, s41
	s_nop 0
	global_load_lds_dwordx4 v[230:231], off
	s_mov_b32 m0, s42
	s_nop 0
	global_load_lds_dwordx4 v[232:233], off
	v_lshl_add_u64 v[232:233], s[0:1], 0, v[134:135]
	s_mov_b32 m0, s43
	s_nop 0
	global_load_lds_dwordx4 v[232:233], off
	s_waitcnt vmcnt(8)
	s_waitcnt lgkmcnt(0)
	s_barrier
	s_setprio 1
	s_waitcnt lgkmcnt(0)
	v_mfma_f32_16x16x32_bf16 v[126:129], v[156:159], v[188:191], v[126:129]
	v_mfma_f32_16x16x32_bf16 v[122:125], v[164:167], v[188:191], v[122:125]
	v_mfma_f32_16x16x32_bf16 v[110:113], v[156:159], v[196:199], v[110:113]
	v_mfma_f32_16x16x32_bf16 v[106:109], v[164:167], v[196:199], v[106:109]
	v_mfma_f32_16x16x32_bf16 v[94:97], v[156:159], v[204:207], v[94:97]
	v_mfma_f32_16x16x32_bf16 v[90:93], v[164:167], v[204:207], v[90:93]
	v_mfma_f32_16x16x32_bf16 v[78:81], v[156:159], v[216:219], v[78:81]
	v_mfma_f32_16x16x32_bf16 v[74:77], v[164:167], v[216:219], v[74:77]
	v_mfma_f32_16x16x32_bf16 v[126:129], v[160:163], v[192:195], v[126:129]
	v_mfma_f32_16x16x32_bf16 v[122:125], v[168:171], v[192:195], v[122:125]
	v_mfma_f32_16x16x32_bf16 v[110:113], v[160:163], v[200:203], v[110:113]
	v_mfma_f32_16x16x32_bf16 v[106:109], v[168:171], v[200:203], v[106:109]
	v_mfma_f32_16x16x32_bf16 v[94:97], v[160:163], v[212:215], v[94:97]
	v_mfma_f32_16x16x32_bf16 v[90:93], v[168:171], v[212:215], v[90:93]
	v_mfma_f32_16x16x32_bf16 v[78:81], v[160:163], v[220:223], v[78:81]
	v_mfma_f32_16x16x32_bf16 v[74:77], v[168:171], v[220:223], v[74:77]
	v_mfma_f32_16x16x32_bf16 v[118:121], v[172:175], v[188:191], v[118:121]
	v_mfma_f32_16x16x32_bf16 v[114:117], v[180:183], v[188:191], v[114:117]
	v_mfma_f32_16x16x32_bf16 v[102:105], v[172:175], v[196:199], v[102:105]
	v_mfma_f32_16x16x32_bf16 v[98:101], v[180:183], v[196:199], v[98:101]
	v_mfma_f32_16x16x32_bf16 v[86:89], v[172:175], v[204:207], v[86:89]
	v_mfma_f32_16x16x32_bf16 v[82:85], v[180:183], v[204:207], v[82:85]
	v_mfma_f32_16x16x32_bf16 v[70:73], v[172:175], v[216:219], v[70:73]
	v_mfma_f32_16x16x32_bf16 v[66:69], v[180:183], v[216:219], v[66:69]
	v_mfma_f32_16x16x32_bf16 v[118:121], v[176:179], v[192:195], v[118:121]
	v_mfma_f32_16x16x32_bf16 v[114:117], v[184:187], v[192:195], v[114:117]
	v_mfma_f32_16x16x32_bf16 v[102:105], v[176:179], v[200:203], v[102:105]
	v_mfma_f32_16x16x32_bf16 v[98:101], v[184:187], v[200:203], v[98:101]
	v_mfma_f32_16x16x32_bf16 v[86:89], v[176:179], v[212:215], v[86:89]
	v_mfma_f32_16x16x32_bf16 v[82:85], v[184:187], v[212:215], v[82:85]
	v_mfma_f32_16x16x32_bf16 v[70:73], v[176:179], v[220:223], v[70:73]
	v_mfma_f32_16x16x32_bf16 v[66:69], v[184:187], v[220:223], v[66:69]
	s_barrier
	s_setprio 0
	s_add_i32 s0, s33, s39
	v_lshl_add_u64 v[148:149], v[148:149], 0, s[22:23]
	s_mov_b32 m0, s0
	ds_read_b128 v[188:191], v154 offset:49152
	ds_read_b128 v[192:195], v154 offset:50176
	ds_read_b128 v[196:199], v154 offset:51200
	ds_read_b128 v[200:203], v154 offset:52224
	ds_read_b128 v[204:207], v154 offset:53248
	ds_read_b128 v[212:215], v154 offset:54272
	ds_read_b128 v[216:219], v154 offset:55296
	ds_read_b128 v[220:223], v154 offset:56320
	global_load_lds_dwordx4 v[148:149], off
	v_lshl_add_u64 v[148:149], v[208:209], 0, s[22:23]
	s_add_i32 m0, s0, 0x2000
	s_add_i32 s0, s63, s39
	global_load_lds_dwordx4 v[148:149], off
	v_lshl_add_u64 v[148:149], v[224:225], 0, s[22:23]
	s_mov_b32 m0, s0
	s_nop 0
	global_load_lds_dwordx4 v[148:149], off
	v_lshl_add_u64 v[148:149], v[226:227], 0, s[22:23]
	s_add_i32 m0, s0, 0x2000
	s_nop 0
	global_load_lds_dwordx4 v[148:149], off
	s_cmp_ge_i32 s61, s47
	s_cbranch_scc0 .Lkr3_b
	v_lshl_add_u64 v[148:149], v[228:229], 0, s[22:23]
	s_mov_b32 m0, s45
	s_nop 0
	global_load_lds_dwordx4 v[148:149], off
	v_lshl_add_u64 v[148:149], v[230:231], 0, s[22:23]
	s_mov_b32 m0, s46
	s_nop 0
	global_load_lds_dwordx4 v[148:149], off
; #define PG8_STAGE(bufoff, gbase, voff) do { _Pragma("unroll") for (int _i = 0; _i < 2; ++_i) \
;         __builtin_amdgcn_global_load_lds((const unsigned*)((const char*)(gbase) + (voff)[_i]), (PG8_LAS unsigned*)(lds + (bufoff) + ldsw + _i * 8192), 16, 0, 0); } while (0)
; #define PG8_LDA(dst, b, h) do { _Pragma("unroll") for (int m = 0; m < 4; ++m) { const bf16x8 f0_ = *(const PG8_LAS bf16x8*)(lds + PG8_SA(b, h) + aoff + m * 2048), f1_ = *(const PG8_LAS bf16x8*)(lds + PG8_SA(b, h) + aoff + m * 2048 + 1024); dst[m].set(f0_, f1_); } } while (0)
; #define PG8_WAIT_V(n) asm volatile("s_waitcnt vmcnt(" #n ")" ::: "memory")
; #define PG8_WAIT_L(n) asm volatile("s_waitcnt lgkmcnt(" #n ")" ::: "memory")
; #define PG8_BAR __builtin_amdgcn_s_barrier()
; #define PG8_SCHED __builtin_amdgcn_sched_barrier(0)
; template <class Epi, class Sched, bool ALIGN_EPI = false, bool SP2 = false>
; __device__ __forceinline__ void gemm_phase(PG8_LAS unsigned char* lds, const Gemm g, const Sched& S, const Epi& E) {
;     ...
;         for (int t = 0; t < nt; t += 2) {
;             if constexpr (Epi::MIDK) { if (t == (nt >> 1)) E.mid(acc, cur, wr, wc, fr, fq); }
;             const bool last = (t == nt - 2);
;             const char* a1 = cA + (size_t)(t + 1) * kstep;
;             const char* a2 = last ? nA : cA + (size_t)(t + 2) * kstep; const char* b2 = last ? nB : cB + (size_t)(t + 2) * kstep;
;     ...
;             PG8_LDA(At, 1, 1); PG8_STAGE(PG8_SB(1, 0), b3, voffB); PG8_STAGE(PG8_SB(1, 1), b3 + hstepB, voffB); PG8_STAGE(PG8_SA(1, 0), a3, voffA);
;             PG8_WAIT_V(8); PG8_WAIT_L(0); PG8_BAR; PG8_MMA(1, 0, At, B0); PG8_MMA(1, 1, At, B1); PG8_BAR; PG8_SCHED;
.Lkr3_b:
	s_waitcnt vmcnt(6)
	s_waitcnt lgkmcnt(0)
	s_barrier
	s_setprio 1
	s_waitcnt lgkmcnt(0)
	v_mfma_f32_16x16x32_bf16 v[62:65], v[156:159], v[188:191], v[62:65]
	v_mfma_f32_16x16x32_bf16 v[58:61], v[164:167], v[188:191], v[58:61]
	v_mfma_f32_16x16x32_bf16 v[46:49], v[156:159], v[196:199], v[46:49]
	v_mfma_f32_16x16x32_bf16 v[42:45], v[164:167], v[196:199], v[42:45]
	v_mfma_f32_16x16x32_bf16 v[30:33], v[156:159], v[204:207], v[30:33]
	v_mfma_f32_16x16x32_bf16 v[26:29], v[164:167], v[204:207], v[26:29]
	v_mfma_f32_16x16x32_bf16 v[14:17], v[156:159], v[216:219], v[14:17]
	v_mfma_f32_16x16x32_bf16 v[6:9], v[164:167], v[216:219], v[6:9]
	v_mfma_f32_16x16x32_bf16 v[62:65], v[160:163], v[192:195], v[62:65]
	v_mfma_f32_16x16x32_bf16 v[58:61], v[168:171], v[192:195], v[58:61]
	v_mfma_f32_16x16x32_bf16 v[46:49], v[160:163], v[200:203], v[46:49]
	v_mfma_f32_16x16x32_bf16 v[42:45], v[168:171], v[200:203], v[42:45]
	v_mfma_f32_16x16x32_bf16 v[30:33], v[160:163], v[212:215], v[30:33]
	v_mfma_f32_16x16x32_bf16 v[26:29], v[168:171], v[212:215], v[26:29]
	v_mfma_f32_16x16x32_bf16 v[14:17], v[160:163], v[220:223], v[14:17]
	v_mfma_f32_16x16x32_bf16 v[6:9], v[168:171], v[220:223], v[6:9]
	v_mfma_f32_16x16x32_bf16 v[54:57], v[172:175], v[188:191], v[54:57]
	v_mfma_f32_16x16x32_bf16 v[50:53], v[180:183], v[188:191], v[50:53]
	v_mfma_f32_16x16x32_bf16 v[38:41], v[172:175], v[196:199], v[38:41]
	v_mfma_f32_16x16x32_bf16 v[34:37], v[180:183], v[196:199], v[34:37]
	v_mfma_f32_16x16x32_bf16 v[22:25], v[172:175], v[204:207], v[22:25]
	v_mfma_f32_16x16x32_bf16 v[18:21], v[180:183], v[204:207], v[18:21]
	v_mfma_f32_16x16x32_bf16 v[10:13], v[172:175], v[216:219], v[10:13]
	v_mfma_f32_16x16x32_bf16 v[2:5], v[180:183], v[216:219], v[2:5]
	v_mfma_f32_16x16x32_bf16 v[54:57], v[176:179], v[192:195], v[54:57]
	v_mfma_f32_16x16x32_bf16 v[50:53], v[184:187], v[192:195], v[50:53]
	v_mfma_f32_16x16x32_bf16 v[38:41], v[176:179], v[200:203], v[38:41]
	v_mfma_f32_16x16x32_bf16 v[34:37], v[184:187], v[200:203], v[34:37]
	v_mfma_f32_16x16x32_bf16 v[22:25], v[176:179], v[212:215], v[22:25]
	v_mfma_f32_16x16x32_bf16 v[18:21], v[184:187], v[212:215], v[18:21]
	v_mfma_f32_16x16x32_bf16 v[10:13], v[176:179], v[220:223], v[10:13]
	v_mfma_f32_16x16x32_bf16 v[2:5], v[184:187], v[220:223], v[2:5]
	s_barrier
	s_setprio 0
	s_add_u32 s30, s30, 0x100
	s_addc_u32 s31, s31, 0
	s_add_u32 s58, s58, 0x100
	s_addc_u32 s59, s59, 0
	s_cmp_ge_i32 s61, s47
	s_cselect_b32 s99, 0, 1
	s_mov_b32 s34, s61
	s_cbranch_scc0 .LBB0_1171

; #define PG8_STAGE(bufoff, gbase, voff) do { _Pragma("unroll") for (int _i = 0; _i < 2; ++_i) \
;         __builtin_amdgcn_global_load_lds((const unsigned*)((const char*)(gbase) + (voff)[_i]), (PG8_LAS unsigned*)(lds + (bufoff) + ldsw + _i * 8192), 16, 0, 0); } while (0)
; #define PG8_LDA(dst, b, h) do { _Pragma("unroll") for (int m = 0; m < 4; ++m) { const bf16x8 f0_ = *(const PG8_LAS bf16x8*)(lds + PG8_SA(b, h) + aoff + m * 2048), f1_ = *(const PG8_LAS bf16x8*)(lds + PG8_SA(b, h) + aoff + m * 2048 + 1024); dst[m].set(f0_, f1_); } } while (0)
; #define PG8_LDB(dst, b, h) do { _Pragma("unroll") for (int n = 0; n < 2; ++n) { const bf16x8 f0_ = *(const PG8_LAS bf16x8*)(lds + PG8_SB(b, h) + boff + n * 2048), f1_ = *(const PG8_LAS bf16x8*)(lds + PG8_SB(b, h) + boff + n * 2048 + 1024); dst[n].set(f0_, f1_); } } while (0)
; #define PG8_WAIT_V(n) asm volatile("s_waitcnt vmcnt(" #n ")" ::: "memory")
; #define PG8_WAIT_L(n) asm volatile("s_waitcnt lgkmcnt(" #n ")" ::: "memory")
; #define PG8_BAR __builtin_amdgcn_s_barrier()
; #define PG8_SCHED __builtin_amdgcn_sched_barrier(0)
; template <class Epi, class Sched, bool ALIGN_EPI = false, bool SP2 = false>
; __device__ __forceinline__ void gemm_phase(PG8_LAS unsigned char* lds, const Gemm g, const Sched& S, const Epi& E) {
;     ...
;             PG8_LDB(B0, 0, 0); PG8_LDB(B1, 0, 1); PG8_SCHED; PG8_LDA(At, 0, 0); PG8_STAGE(PG8_SA(1, 1), a1 + hstep, voffA);
;             PG8_WAIT_V(8); PG8_WAIT_L(0); PG8_BAR; PG8_MMA(0, 0, At, B0); PG8_MMA(0, 1, At, B1); PG8_BAR; PG8_SCHED;
;             PG8_LDA(At, 0, 1); PG8_STAGE(PG8_SB(0, 0), b2, voffB); PG8_STAGE(PG8_SB(0, 1), b2 + hstepB, voffB); PG8_STAGE(PG8_SA(0, 0), a2, voffA);
;             PG8_WAIT_V(8); PG8_WAIT_L(0); PG8_BAR; PG8_MMA(1, 0, At, B0); PG8_MMA(1, 1, At, B1); PG8_BAR; PG8_SCHED;
.Lkr4_a:
	v_lshl_add_u64 v[148:149], s[30:31], 0, v[140:141]
	s_add_i32 m0, s40, 0xc000
	ds_read_b128 v[188:191], v154
	ds_read_b128 v[192:195], v154 offset:1024
	ds_read_b128 v[196:199], v154 offset:2048
	ds_read_b128 v[200:203], v154 offset:3072
	ds_read_b128 v[204:207], v154 offset:4096
	ds_read_b128 v[212:215], v154 offset:5120
	ds_read_b128 v[216:219], v154 offset:6144
	ds_read_b128 v[220:223], v154 offset:7168
	global_load_lds_dwordx4 v[148:149], off
	v_lshl_add_u64 v[148:149], s[30:31], 0, v[142:143]
	s_add_i32 m0, s40, 0xe000
	s_nop 0
	global_load_lds_dwordx4 v[148:149], off
	s_waitcnt vmcnt(8)
	s_waitcnt lgkmcnt(0)
	s_barrier
	s_setprio 1
	s_waitcnt lgkmcnt(0)
	v_mfma_f32_16x16x32_bf16 v[126:129], v[156:159], v[188:191], v[126:129]
	v_mfma_f32_16x16x32_bf16 v[122:125], v[164:167], v[188:191], v[122:125]
	v_mfma_f32_16x16x32_bf16 v[110:113], v[156:159], v[196:199], v[110:113]
	v_mfma_f32_16x16x32_bf16 v[106:109], v[164:167], v[196:199], v[106:109]
	v_mfma_f32_16x16x32_bf16 v[94:97], v[156:159], v[204:207], v[94:97]
	v_mfma_f32_16x16x32_bf16 v[90:93], v[164:167], v[204:207], v[90:93]
	v_mfma_f32_16x16x32_bf16 v[78:81], v[156:159], v[216:219], v[78:81]
	v_mfma_f32_16x16x32_bf16 v[74:77], v[164:167], v[216:219], v[74:77]
	v_mfma_f32_16x16x32_bf16 v[126:129], v[160:163], v[192:195], v[126:129]
	v_mfma_f32_16x16x32_bf16 v[122:125], v[168:171], v[192:195], v[122:125]
	v_mfma_f32_16x16x32_bf16 v[110:113], v[160:163], v[200:203], v[110:113]
	v_mfma_f32_16x16x32_bf16 v[106:109], v[168:171], v[200:203], v[106:109]
	v_mfma_f32_16x16x32_bf16 v[94:97], v[160:163], v[212:215], v[94:97]
	v_mfma_f32_16x16x32_bf16 v[90:93], v[168:171], v[212:215], v[90:93]
	v_mfma_f32_16x16x32_bf16 v[78:81], v[160:163], v[220:223], v[78:81]
	v_mfma_f32_16x16x32_bf16 v[74:77], v[168:171], v[220:223], v[74:77]
	v_mfma_f32_16x16x32_bf16 v[118:121], v[172:175], v[188:191], v[118:121]
	v_mfma_f32_16x16x32_bf16 v[114:117], v[180:183], v[188:191], v[114:117]
	v_mfma_f32_16x16x32_bf16 v[102:105], v[172:175], v[196:199], v[102:105]
	v_mfma_f32_16x16x32_bf16 v[98:101], v[180:183], v[196:199], v[98:101]
	v_mfma_f32_16x16x32_bf16 v[86:89], v[172:175], v[204:207], v[86:89]
	v_mfma_f32_16x16x32_bf16 v[82:85], v[180:183], v[204:207], v[82:85]
	v_mfma_f32_16x16x32_bf16 v[70:73], v[172:175], v[216:219], v[70:73]
	v_mfma_f32_16x16x32_bf16 v[66:69], v[180:183], v[216:219], v[66:69]
	v_mfma_f32_16x16x32_bf16 v[118:121], v[176:179], v[192:195], v[118:121]
	v_mfma_f32_16x16x32_bf16 v[114:117], v[184:187], v[192:195], v[114:117]
	v_mfma_f32_16x16x32_bf16 v[102:105], v[176:179], v[200:203], v[102:105]
	v_mfma_f32_16x16x32_bf16 v[98:101], v[184:187], v[200:203], v[98:101]
	v_mfma_f32_16x16x32_bf16 v[86:89], v[176:179], v[212:215], v[86:89]
	v_mfma_f32_16x16x32_bf16 v[82:85], v[184:187], v[212:215], v[82:85]
	v_mfma_f32_16x16x32_bf16 v[70:73], v[176:179], v[220:223], v[70:73]
	v_mfma_f32_16x16x32_bf16 v[66:69], v[184:187], v[220:223], v[66:69]
	s_barrier
	s_setprio 0
	s_add_i32 s33, s52, s39
	v_lshl_add_u64 v[148:149], s[0:1], 0, v[132:133]
	s_mov_b32 m0, s33
	ds_read_b128 v[188:191], v154 offset:16384
	ds_read_b128 v[192:195], v154 offset:17408
	ds_read_b128 v[196:199], v154 offset:18432
	ds_read_b128 v[200:203], v154 offset:19456
	ds_read_b128 v[204:207], v154 offset:20480
	ds_read_b128 v[212:215], v154 offset:21504
	ds_read_b128 v[216:219], v154 offset:22528
	ds_read_b128 v[220:223], v154 offset:23552
	global_load_lds_dwordx4 v[148:149], off
	s_add_i32 m0, s33, 0x2000
	v_lshl_add_u64 v[208:209], s[0:1], 0, v[136:137]
	s_add_u32 s0, s0, s14
	s_addc_u32 s1, s1, s15
	s_add_i32 s33, s53, s39
	global_load_lds_dwordx4 v[208:209], off
	v_lshl_add_u64 v[224:225], s[0:1], 0, v[132:133]
	s_mov_b32 m0, s33
	v_lshl_add_u64 v[226:227], s[0:1], 0, v[136:137]
	global_load_lds_dwordx4 v[224:225], off
	s_add_i32 m0, s33, 0x2000
	v_lshl_add_u64 v[228:229], s[34:35], 0, v[130:131]
	global_load_lds_dwordx4 v[226:227], off
	v_lshl_add_u64 v[230:231], s[34:35], 0, v[134:135]
	s_waitcnt vmcnt(6)
	s_waitcnt lgkmcnt(0)
	s_barrier
	s_setprio 1
	s_waitcnt lgkmcnt(0)
	v_mfma_f32_16x16x32_bf16 v[62:65], v[156:159], v[188:191], v[62:65]
	v_mfma_f32_16x16x32_bf16 v[58:61], v[164:167], v[188:191], v[58:61]
	v_mfma_f32_16x16x32_bf16 v[46:49], v[156:159], v[196:199], v[46:49]
	v_mfma_f32_16x16x32_bf16 v[42:45], v[164:167], v[196:199], v[42:45]
	v_mfma_f32_16x16x32_bf16 v[30:33], v[156:159], v[204:207], v[30:33]
	v_mfma_f32_16x16x32_bf16 v[26:29], v[164:167], v[204:207], v[26:29]
	v_mfma_f32_16x16x32_bf16 v[14:17], v[156:159], v[216:219], v[14:17]
	v_mfma_f32_16x16x32_bf16 v[6:9], v[164:167], v[216:219], v[6:9]
	v_mfma_f32_16x16x32_bf16 v[62:65], v[160:163], v[192:195], v[62:65]
	v_mfma_f32_16x16x32_bf16 v[58:61], v[168:171], v[192:195], v[58:61]
	v_mfma_f32_16x16x32_bf16 v[46:49], v[160:163], v[200:203], v[46:49]
	v_mfma_f32_16x16x32_bf16 v[42:45], v[168:171], v[200:203], v[42:45]
	v_mfma_f32_16x16x32_bf16 v[30:33], v[160:163], v[212:215], v[30:33]
	v_mfma_f32_16x16x32_bf16 v[26:29], v[168:171], v[212:215], v[26:29]
	v_mfma_f32_16x16x32_bf16 v[14:17], v[160:163], v[220:223], v[14:17]
	v_mfma_f32_16x16x32_bf16 v[6:9], v[168:171], v[220:223], v[6:9]
	v_mfma_f32_16x16x32_bf16 v[54:57], v[172:175], v[188:191], v[54:57]
	v_mfma_f32_16x16x32_bf16 v[50:53], v[180:183], v[188:191], v[50:53]
	v_mfma_f32_16x16x32_bf16 v[38:41], v[172:175], v[196:199], v[38:41]
	v_mfma_f32_16x16x32_bf16 v[34:37], v[180:183], v[196:199], v[34:37]
	v_mfma_f32_16x16x32_bf16 v[22:25], v[172:175], v[204:207], v[22:25]
	v_mfma_f32_16x16x32_bf16 v[18:21], v[180:183], v[204:207], v[18:21]
	v_mfma_f32_16x16x32_bf16 v[10:13], v[172:175], v[216:219], v[10:13]
	v_mfma_f32_16x16x32_bf16 v[2:5], v[180:183], v[216:219], v[2:5]
	v_mfma_f32_16x16x32_bf16 v[54:57], v[176:179], v[192:195], v[54:57]
	v_mfma_f32_16x16x32_bf16 v[50:53], v[184:187], v[192:195], v[50:53]
	v_mfma_f32_16x16x32_bf16 v[38:41], v[176:179], v[200:203], v[38:41]
	v_mfma_f32_16x16x32_bf16 v[34:37], v[184:187], v[200:203], v[34:37]
	v_mfma_f32_16x16x32_bf16 v[22:25], v[176:179], v[212:215], v[22:25]
	v_mfma_f32_16x16x32_bf16 v[18:21], v[184:187], v[212:215], v[18:21]
	v_mfma_f32_16x16x32_bf16 v[10:13], v[176:179], v[220:223], v[10:13]
	v_mfma_f32_16x16x32_bf16 v[2:5], v[184:187], v[220:223], v[2:5]
	s_barrier
; #define PG8_STAGE(bufoff, gbase, voff) do { _Pragma("unroll") for (int _i = 0; _i < 2; ++_i) \
;         __builtin_amdgcn_global_load_lds((const unsigned*)((const char*)(gbase) + (voff)[_i]), (PG8_LAS unsigned*)(lds + (bufoff) + ldsw + _i * 8192), 16, 0, 0); } while (0)
; #define PG8_LDA(dst, b, h) do { _Pragma("unroll") for (int m = 0; m < 4; ++m) { const bf16x8 f0_ = *(const PG8_LAS bf16x8*)(lds + PG8_SA(b, h) + aoff + m * 2048), f1_ = *(const PG8_LAS bf16x8*)(lds + PG8_SA(b, h) + aoff + m * 2048 + 1024); dst[m].set(f0_, f1_); } } while (0)
; #define PG8_LDB(dst, b, h) do { _Pragma("unroll") for (int n = 0; n < 2; ++n) { const bf16x8 f0_ = *(const PG8_LAS bf16x8*)(lds + PG8_SB(b, h) + boff + n * 2048), f1_ = *(const PG8_LAS bf16x8*)(lds + PG8_SB(b, h) + boff + n * 2048 + 1024); dst[n].set(f0_, f1_); } } while (0)
; #define PG8_WAIT_V(n) asm volatile("s_waitcnt vmcnt(" #n ")" ::: "memory")
; #define PG8_WAIT_L(n) asm volatile("s_waitcnt lgkmcnt(" #n ")" ::: "memory")
; #define PG8_BAR __builtin_amdgcn_s_barrier()
; #define PG8_SCHED __builtin_amdgcn_sched_barrier(0)
; template <class Epi, class Sched, bool ALIGN_EPI = false, bool SP2 = false>
; __device__ __forceinline__ void gemm_phase(PG8_LAS unsigned char* lds, const Gemm g, const Sched& S, const Epi& E) {
;     ...
;             PG8_LDB(B0, 1, 0); PG8_LDB(B1, 1, 1); PG8_SCHED; PG8_LDA(At, 1, 0); PG8_STAGE(PG8_SA(0, 1), a2 + hstep, voffA);
;             PG8_WAIT_V(8); PG8_WAIT_L(0); PG8_BAR; PG8_MMA(0, 0, At, B0); PG8_MMA(0, 1, At, B1); PG8_BAR; PG8_SCHED;
;             PG8_LDA(At, 1, 1); PG8_STAGE(PG8_SB(1, 0), b3, voffB); PG8_STAGE(PG8_SB(1, 1), b3 + hstepB, voffB); PG8_STAGE(PG8_SA(1, 0), a3, voffA);
;             PG8_WAIT_V(8); PG8_WAIT_L(0); PG8_BAR; PG8_MMA(1, 0, At, B0); PG8_MMA(1, 1, At, B1); PG8_BAR; PG8_SCHED;
	s_setprio 0
	s_add_i32 s33, 0, 0x18000
	s_add_i32 s63, 0, 0x1c000
	v_add_u32_e32 v168, s33, v1
	v_add_u32_e32 v184, s63, v1
	ds_read_b128 v[156:159], v168
	ds_read_b128 v[160:163], v168 offset:1024
	ds_read_b128 v[164:167], v168 offset:2048
	ds_read_b128 v[168:171], v168 offset:3072
	ds_read_b128 v[172:175], v184
	ds_read_b128 v[176:179], v184 offset:1024
	ds_read_b128 v[180:183], v184 offset:2048
	ds_read_b128 v[184:187], v184 offset:3072
	s_add_u32 s0, s34, s12
	s_addc_u32 s1, s35, s13
	s_mov_b32 m0, s42
	v_lshl_add_u64 v[232:233], s[0:1], 0, v[130:131]
	ds_read_b128 v[188:191], v154 offset:32768
	ds_read_b128 v[192:195], v154 offset:33792
	ds_read_b128 v[196:199], v154 offset:34816
	ds_read_b128 v[200:203], v154 offset:35840
	ds_read_b128 v[204:207], v154 offset:36864
	ds_read_b128 v[212:215], v154 offset:37888
	ds_read_b128 v[216:219], v154 offset:38912
	ds_read_b128 v[220:223], v154 offset:39936
	s_mov_b32 m0, s40
	s_nop 0
	global_load_lds_dwordx4 v[228:229], off
	s_mov_b32 m0, s41
	s_nop 0
	global_load_lds_dwordx4 v[230:231], off
	s_mov_b32 m0, s42
	s_nop 0
	global_load_lds_dwordx4 v[232:233], off
	v_lshl_add_u64 v[232:233], s[0:1], 0, v[134:135]
	s_mov_b32 m0, s43
	s_nop 0
	global_load_lds_dwordx4 v[232:233], off
	s_waitcnt vmcnt(8)
	s_waitcnt lgkmcnt(0)
	s_barrier
	s_setprio 1
	s_waitcnt lgkmcnt(0)
	v_mfma_f32_16x16x32_bf16 v[126:129], v[156:159], v[188:191], v[126:129]
	v_mfma_f32_16x16x32_bf16 v[122:125], v[164:167], v[188:191], v[122:125]
	v_mfma_f32_16x16x32_bf16 v[110:113], v[156:159], v[196:199], v[110:113]
	v_mfma_f32_16x16x32_bf16 v[106:109], v[164:167], v[196:199], v[106:109]
	v_mfma_f32_16x16x32_bf16 v[94:97], v[156:159], v[204:207], v[94:97]
	v_mfma_f32_16x16x32_bf16 v[90:93], v[164:167], v[204:207], v[90:93]
	v_mfma_f32_16x16x32_bf16 v[78:81], v[156:159], v[216:219], v[78:81]
	v_mfma_f32_16x16x32_bf16 v[74:77], v[164:167], v[216:219], v[74:77]
	v_mfma_f32_16x16x32_bf16 v[126:129], v[160:163], v[192:195], v[126:129]
	v_mfma_f32_16x16x32_bf16 v[122:125], v[168:171], v[192:195], v[122:125]
	v_mfma_f32_16x16x32_bf16 v[110:113], v[160:163], v[200:203], v[110:113]
	v_mfma_f32_16x16x32_bf16 v[106:109], v[168:171], v[200:203], v[106:109]
	v_mfma_f32_16x16x32_bf16 v[94:97], v[160:163], v[212:215], v[94:97]
	v_mfma_f32_16x16x32_bf16 v[90:93], v[168:171], v[212:215], v[90:93]
	v_mfma_f32_16x16x32_bf16 v[78:81], v[160:163], v[220:223], v[78:81]
	v_mfma_f32_16x16x32_bf16 v[74:77], v[168:171], v[220:223], v[74:77]
	v_mfma_f32_16x16x32_bf16 v[118:121], v[172:175], v[188:191], v[118:121]
	v_mfma_f32_16x16x32_bf16 v[114:117], v[180:183], v[188:191], v[114:117]
	v_mfma_f32_16x16x32_bf16 v[102:105], v[172:175], v[196:199], v[102:105]
	v_mfma_f32_16x16x32_bf16 v[98:101], v[180:183], v[196:199], v[98:101]
	v_mfma_f32_16x16x32_bf16 v[86:89], v[172:175], v[204:207], v[86:89]
	v_mfma_f32_16x16x32_bf16 v[82:85], v[180:183], v[204:207], v[82:85]
	v_mfma_f32_16x16x32_bf16 v[70:73], v[172:175], v[216:219], v[70:73]
	v_mfma_f32_16x16x32_bf16 v[66:69], v[180:183], v[216:219], v[66:69]
	v_mfma_f32_16x16x32_bf16 v[118:121], v[176:179], v[192:195], v[118:121]
	v_mfma_f32_16x16x32_bf16 v[114:117], v[184:187], v[192:195], v[114:117]
	v_mfma_f32_16x16x32_bf16 v[102:105], v[176:179], v[200:203], v[102:105]
	v_mfma_f32_16x16x32_bf16 v[98:101], v[184:187], v[200:203], v[98:101]
	v_mfma_f32_16x16x32_bf16 v[86:89], v[176:179], v[212:215], v[86:89]
	v_mfma_f32_16x16x32_bf16 v[82:85], v[184:187], v[212:215], v[82:85]
	v_mfma_f32_16x16x32_bf16 v[70:73], v[176:179], v[220:223], v[70:73]
	v_mfma_f32_16x16x32_bf16 v[66:69], v[184:187], v[220:223], v[66:69]
	s_barrier
	s_setprio 0
	s_add_i32 s0, s33, s39
	v_lshl_add_u64 v[148:149], v[148:149], 0, s[22:23]
	s_mov_b32 m0, s0
	ds_read_b128 v[188:191], v154 offset:49152
	ds_read_b128 v[192:195], v154 offset:50176
	ds_read_b128 v[196:199], v154 offset:51200
	ds_read_b128 v[200:203], v154 offset:52224
	ds_read_b128 v[204:207], v154 offset:53248
	ds_read_b128 v[212:215], v154 offset:54272
	ds_read_b128 v[216:219], v154 offset:55296
	ds_read_b128 v[220:223], v154 offset:56320
	global_load_lds_dwordx4 v[148:149], off
	v_lshl_add_u64 v[148:149], v[208:209], 0, s[22:23]
	s_add_i32 m0, s0, 0x2000
	s_add_i32 s0, s63, s39
	global_load_lds_dwordx4 v[148:149], off
	v_lshl_add_u64 v[148:149], v[224:225], 0, s[22:23]
	s_mov_b32 m0, s0
	s_nop 0
	global_load_lds_dwordx4 v[148:149], off
	v_lshl_add_u64 v[148:149], v[226:227], 0, s[22:23]
	s_add_i32 m0, s0, 0x2000
	s_nop 0
	global_load_lds_dwordx4 v[148:149], off
	s_cmp_ge_i32 s61, s48
	s_cbranch_scc0 .Lkr4_b
	v_lshl_add_u64 v[148:149], v[228:229], 0, s[22:23]
	s_mov_b32 m0, s46
	s_nop 0
	global_load_lds_dwordx4 v[148:149], off
	v_lshl_add_u64 v[148:149], v[230:231], 0, s[22:23]
	s_mov_b32 m0, s47
	s_nop 0
	global_load_lds_dwordx4 v[148:149], off
; #define PG8_STAGE(bufoff, gbase, voff) do { _Pragma("unroll") for (int _i = 0; _i < 2; ++_i) \
;         __builtin_amdgcn_global_load_lds((const unsigned*)((const char*)(gbase) + (voff)[_i]), (PG8_LAS unsigned*)(lds + (bufoff) + ldsw + _i * 8192), 16, 0, 0); } while (0)
; #define PG8_LDA(dst, b, h) do { _Pragma("unroll") for (int m = 0; m < 4; ++m) { const bf16x8 f0_ = *(const PG8_LAS bf16x8*)(lds + PG8_SA(b, h) + aoff + m * 2048), f1_ = *(const PG8_LAS bf16x8*)(lds + PG8_SA(b, h) + aoff + m * 2048 + 1024); dst[m].set(f0_, f1_); } } while (0)
; #define PG8_WAIT_V(n) asm volatile("s_waitcnt vmcnt(" #n ")" ::: "memory")
; #define PG8_WAIT_L(n) asm volatile("s_waitcnt lgkmcnt(" #n ")" ::: "memory")
; #define PG8_BAR __builtin_amdgcn_s_barrier()
; #define PG8_SCHED __builtin_amdgcn_sched_barrier(0)
; template <class Epi, class Sched, bool ALIGN_EPI = false, bool SP2 = false>
; __device__ __forceinline__ void gemm_phase(PG8_LAS unsigned char* lds, const Gemm g, const Sched& S, const Epi& E) {
;     ...
;         for (int t = 0; t < nt; t += 2) {
;             if constexpr (Epi::MIDK) { if (t == (nt >> 1)) E.mid(acc, cur, wr, wc, fr, fq); }
;             const bool last = (t == nt - 2);
;             const char* a1 = cA + (size_t)(t + 1) * kstep;
;             const char* a2 = last ? nA : cA + (size_t)(t + 2) * kstep; const char* b2 = last ? nB : cB + (size_t)(t + 2) * kstep;
;     ...
;             PG8_LDA(At, 1, 1); PG8_STAGE(PG8_SB(1, 0), b3, voffB); PG8_STAGE(PG8_SB(1, 1), b3 + hstepB, voffB); PG8_STAGE(PG8_SA(1, 0), a3, voffA);
;             PG8_WAIT_V(8); PG8_WAIT_L(0); PG8_BAR; PG8_MMA(1, 0, At, B0); PG8_MMA(1, 1, At, B1); PG8_BAR; PG8_SCHED;
.Lkr4_b:
	s_waitcnt vmcnt(6)
	s_waitcnt lgkmcnt(0)
	s_barrier
	s_setprio 1
	s_waitcnt lgkmcnt(0)
	v_mfma_f32_16x16x32_bf16 v[62:65], v[156:159], v[188:191], v[62:65]
	v_mfma_f32_16x16x32_bf16 v[58:61], v[164:167], v[188:191], v[58:61]
	v_mfma_f32_16x16x32_bf16 v[46:49], v[156:159], v[196:199], v[46:49]
	v_mfma_f32_16x16x32_bf16 v[42:45], v[164:167], v[196:199], v[42:45]
	v_mfma_f32_16x16x32_bf16 v[30:33], v[156:159], v[204:207], v[30:33]
	v_mfma_f32_16x16x32_bf16 v[26:29], v[164:167], v[204:207], v[26:29]
	v_mfma_f32_16x16x32_bf16 v[14:17], v[156:159], v[216:219], v[14:17]
	v_mfma_f32_16x16x32_bf16 v[6:9], v[164:167], v[216:219], v[6:9]
	v_mfma_f32_16x16x32_bf16 v[62:65], v[160:163], v[192:195], v[62:65]
	v_mfma_f32_16x16x32_bf16 v[58:61], v[168:171], v[192:195], v[58:61]
	v_mfma_f32_16x16x32_bf16 v[46:49], v[160:163], v[200:203], v[46:49]
	v_mfma_f32_16x16x32_bf16 v[42:45], v[168:171], v[200:203], v[42:45]
	v_mfma_f32_16x16x32_bf16 v[30:33], v[160:163], v[212:215], v[30:33]
	v_mfma_f32_16x16x32_bf16 v[26:29], v[168:171], v[212:215], v[26:29]
	v_mfma_f32_16x16x32_bf16 v[14:17], v[160:163], v[220:223], v[14:17]
	v_mfma_f32_16x16x32_bf16 v[6:9], v[168:171], v[220:223], v[6:9]
	v_mfma_f32_16x16x32_bf16 v[54:57], v[172:175], v[188:191], v[54:57]
	v_mfma_f32_16x16x32_bf16 v[50:53], v[180:183], v[188:191], v[50:53]
	v_mfma_f32_16x16x32_bf16 v[38:41], v[172:175], v[196:199], v[38:41]
	v_mfma_f32_16x16x32_bf16 v[34:37], v[180:183], v[196:199], v[34:37]
	v_mfma_f32_16x16x32_bf16 v[22:25], v[172:175], v[204:207], v[22:25]
	v_mfma_f32_16x16x32_bf16 v[18:21], v[180:183], v[204:207], v[18:21]
	v_mfma_f32_16x16x32_bf16 v[10:13], v[172:175], v[216:219], v[10:13]
	v_mfma_f32_16x16x32_bf16 v[2:5], v[180:183], v[216:219], v[2:5]
	v_mfma_f32_16x16x32_bf16 v[54:57], v[176:179], v[192:195], v[54:57]
	v_mfma_f32_16x16x32_bf16 v[50:53], v[184:187], v[192:195], v[50:53]
	v_mfma_f32_16x16x32_bf16 v[38:41], v[176:179], v[200:203], v[38:41]
	v_mfma_f32_16x16x32_bf16 v[34:37], v[184:187], v[200:203], v[34:37]
	v_mfma_f32_16x16x32_bf16 v[22:25], v[176:179], v[212:215], v[22:25]
	v_mfma_f32_16x16x32_bf16 v[18:21], v[184:187], v[212:215], v[18:21]
	v_mfma_f32_16x16x32_bf16 v[10:13], v[176:179], v[220:223], v[10:13]
	v_mfma_f32_16x16x32_bf16 v[2:5], v[184:187], v[220:223], v[2:5]
	s_barrier
	s_setprio 0
	s_add_u32 s30, s30, 0x100
	s_addc_u32 s31, s31, 0
	s_add_u32 s58, s58, 0x100
	s_addc_u32 s59, s59, 0
	s_cmp_ge_i32 s61, s48
	s_cselect_b32 s99, 0, 1
	s_mov_b32 s34, s61
	s_cbranch_scc0 .LBB0_1592

; #define PG8_STAGE(bufoff, gbase, voff) do { _Pragma("unroll") for (int _i = 0; _i < 2; ++_i) \
;         __builtin_amdgcn_global_load_lds((const unsigned*)((const char*)(gbase) + (voff)[_i]), (PG8_LAS unsigned*)(lds + (bufoff) + ldsw + _i * 8192), 16, 0, 0); } while (0)
; #define PG8_LDA(dst, b, h) do { _Pragma("unroll") for (int m = 0; m < 4; ++m) { const bf16x8 f0_ = *(const PG8_LAS bf16x8*)(lds + PG8_SA(b, h) + aoff + m * 2048), f1_ = *(const PG8_LAS bf16x8*)(lds + PG8_SA(b, h) + aoff + m * 2048 + 1024); dst[m].set(f0_, f1_); } } while (0)
; #define PG8_LDB(dst, b, h) do { _Pragma("unroll") for (int n = 0; n < 2; ++n) { const bf16x8 f0_ = *(const PG8_LAS bf16x8*)(lds + PG8_SB(b, h) + boff + n * 2048), f1_ = *(const PG8_LAS bf16x8*)(lds + PG8_SB(b, h) + boff + n * 2048 + 1024); dst[n].set(f0_, f1_); } } while (0)
; #define PG8_WAIT_V(n) asm volatile("s_waitcnt vmcnt(" #n ")" ::: "memory")
; #define PG8_WAIT_L(n) asm volatile("s_waitcnt lgkmcnt(" #n ")" ::: "memory")
; #define PG8_BAR __builtin_amdgcn_s_barrier()
; #define PG8_SCHED __builtin_amdgcn_sched_barrier(0)
; template <class Epi, class Sched, bool ALIGN_EPI = false, bool SP2 = false>
; __device__ __forceinline__ void gemm_phase(PG8_LAS unsigned char* lds, const Gemm g, const Sched& S, const Epi& E) {
;     ...
;             PG8_LDB(B0, 0, 0); PG8_LDB(B1, 0, 1); PG8_SCHED; PG8_LDA(At, 0, 0); PG8_STAGE(PG8_SA(1, 1), a1 + hstep, voffA);
;             PG8_WAIT_V(8); PG8_WAIT_L(0); PG8_BAR; PG8_MMA(0, 0, At, B0); PG8_MMA(0, 1, At, B1); PG8_BAR; PG8_SCHED;
;             PG8_LDA(At, 0, 1); PG8_STAGE(PG8_SB(0, 0), b2, voffB); PG8_STAGE(PG8_SB(0, 1), b2 + hstepB, voffB); PG8_STAGE(PG8_SA(0, 0), a2, voffA);
;             PG8_WAIT_V(8); PG8_WAIT_L(0); PG8_BAR; PG8_MMA(1, 0, At, B0); PG8_MMA(1, 1, At, B1); PG8_BAR; PG8_SCHED;
.Lkr5_a:
	v_lshl_add_u64 v[192:193], s[46:47], 0, v[176:177]
	s_add_i32 m0, s10, 0xc000
	ds_read_b128 v[184:187], v199
	ds_read_b128 v[188:191], v199 offset:1024
	ds_read_b128 v[212:215], v199 offset:2048
	ds_read_b128 v[216:219], v199 offset:3072
	ds_read_b128 v[220:223], v199 offset:4096
	ds_read_b128 v[224:227], v199 offset:5120
	ds_read_b128 v[228:231], v199 offset:6144
	ds_read_b128 v[232:235], v199 offset:7168
	global_load_lds_dwordx4 v[192:193], off
	v_lshl_add_u64 v[192:193], s[46:47], 0, v[178:179]
	s_add_i32 m0, s10, 0xe000
	s_nop 0
	global_load_lds_dwordx4 v[192:193], off
	s_waitcnt vmcnt(8)
	s_waitcnt lgkmcnt(0)
	s_barrier
	s_setprio 1
	s_waitcnt lgkmcnt(0)
	v_mfma_scale_f32_16x16x128_f8f6f4 v[158:161], v[18:25], v[184:191], v[158:161], v200, v201 op_sel_hi:[0,0,0]
	v_mfma_scale_f32_16x16x128_f8f6f4 v[154:157], v[26:33], v[184:191], v[154:157], v200, v201 op_sel_hi:[0,0,0]
	v_mfma_scale_f32_16x16x128_f8f6f4 v[142:145], v[18:25], v[212:219], v[142:145], v200, v201 op_sel_hi:[0,0,0]
	v_mfma_scale_f32_16x16x128_f8f6f4 v[138:141], v[26:33], v[212:219], v[138:141], v200, v201 op_sel_hi:[0,0,0]
	v_mfma_scale_f32_16x16x128_f8f6f4 v[126:129], v[18:25], v[220:227], v[126:129], v200, v201 op_sel_hi:[0,0,0]
	v_mfma_scale_f32_16x16x128_f8f6f4 v[122:125], v[26:33], v[220:227], v[122:125], v200, v201 op_sel_hi:[0,0,0]
	v_mfma_scale_f32_16x16x128_f8f6f4 v[110:113], v[18:25], v[228:235], v[110:113], v200, v201 op_sel_hi:[0,0,0]
	v_mfma_scale_f32_16x16x128_f8f6f4 v[106:109], v[26:33], v[228:235], v[106:109], v200, v201 op_sel_hi:[0,0,0]
	v_mfma_scale_f32_16x16x128_f8f6f4 v[150:153], v[2:9], v[184:191], v[150:153], v200, v201 op_sel_hi:[0,0,0]
	v_mfma_scale_f32_16x16x128_f8f6f4 v[146:149], v[10:17], v[184:191], v[146:149], v200, v201 op_sel_hi:[0,0,0]
	v_mfma_scale_f32_16x16x128_f8f6f4 v[134:137], v[2:9], v[212:219], v[134:137], v200, v201 op_sel_hi:[0,0,0]
	v_mfma_scale_f32_16x16x128_f8f6f4 v[130:133], v[10:17], v[212:219], v[130:133], v200, v201 op_sel_hi:[0,0,0]
	v_mfma_scale_f32_16x16x128_f8f6f4 v[118:121], v[2:9], v[220:227], v[118:121], v200, v201 op_sel_hi:[0,0,0]
	v_mfma_scale_f32_16x16x128_f8f6f4 v[114:117], v[10:17], v[220:227], v[114:117], v200, v201 op_sel_hi:[0,0,0]
	v_mfma_scale_f32_16x16x128_f8f6f4 v[102:105], v[2:9], v[228:235], v[102:105], v200, v201 op_sel_hi:[0,0,0]
	v_mfma_scale_f32_16x16x128_f8f6f4 v[98:101], v[10:17], v[228:235], v[98:101], v200, v201 op_sel_hi:[0,0,0]
	s_barrier
	s_setprio 0
	s_add_i32 s0, s73, s9
	v_lshl_add_u64 v[184:185], s[50:51], 0, v[164:165]
	s_mov_b32 m0, s0
	ds_read_b128 v[212:215], v199 offset:16384
	ds_read_b128 v[216:219], v199 offset:17408
	ds_read_b128 v[220:223], v199 offset:18432
	ds_read_b128 v[224:227], v199 offset:19456
	ds_read_b128 v[228:231], v199 offset:20480
	ds_read_b128 v[232:235], v199 offset:21504
	ds_read_b128 v[236:239], v199 offset:22528
	ds_read_b128 v[240:243], v199 offset:23552
	global_load_lds_dwordx4 v[184:185], off
	s_add_i32 m0, s0, 0x2000
	s_add_u32 s0, s50, s14
	v_lshl_add_u64 v[186:187], s[50:51], 0, v[168:169]
	s_addc_u32 s1, s51, s15
	s_add_i32 s33, s74, s9
	global_load_lds_dwordx4 v[186:187], off
	v_lshl_add_u64 v[188:189], s[0:1], 0, v[164:165]
	s_mov_b32 m0, s33
	v_lshl_add_u64 v[190:191], s[0:1], 0, v[168:169]
	global_load_lds_dwordx4 v[188:189], off
	s_add_i32 m0, s33, 0x2000
	v_lshl_add_u64 v[192:193], s[48:49], 0, v[162:163]
	global_load_lds_dwordx4 v[190:191], off
	v_lshl_add_u64 v[194:195], s[48:49], 0, v[166:167]
	s_waitcnt vmcnt(6)
	s_waitcnt lgkmcnt(0)
	s_barrier
	s_setprio 1
	s_waitcnt lgkmcnt(0)
	v_mfma_scale_f32_16x16x128_f8f6f4 v[94:97], v[18:25], v[212:219], v[94:97], v200, v201 op_sel_hi:[0,0,0]
	v_mfma_scale_f32_16x16x128_f8f6f4 v[90:93], v[26:33], v[212:219], v[90:93], v200, v201 op_sel_hi:[0,0,0]
	v_mfma_scale_f32_16x16x128_f8f6f4 v[78:81], v[18:25], v[220:227], v[78:81], v200, v201 op_sel_hi:[0,0,0]
	v_mfma_scale_f32_16x16x128_f8f6f4 v[74:77], v[26:33], v[220:227], v[74:77], v200, v201 op_sel_hi:[0,0,0]
	v_mfma_scale_f32_16x16x128_f8f6f4 v[62:65], v[18:25], v[228:235], v[62:65], v200, v201 op_sel_hi:[0,0,0]
	v_mfma_scale_f32_16x16x128_f8f6f4 v[58:61], v[26:33], v[228:235], v[58:61], v200, v201 op_sel_hi:[0,0,0]
	v_mfma_scale_f32_16x16x128_f8f6f4 v[46:49], v[18:25], v[236:243], v[46:49], v200, v201 op_sel_hi:[0,0,0]
	v_mfma_scale_f32_16x16x128_f8f6f4 v[42:45], v[26:33], v[236:243], v[42:45], v200, v201 op_sel_hi:[0,0,0]
	v_mfma_scale_f32_16x16x128_f8f6f4 v[86:89], v[2:9], v[212:219], v[86:89], v200, v201 op_sel_hi:[0,0,0]
	v_mfma_scale_f32_16x16x128_f8f6f4 v[82:85], v[10:17], v[212:219], v[82:85], v200, v201 op_sel_hi:[0,0,0]
	v_mfma_scale_f32_16x16x128_f8f6f4 v[70:73], v[2:9], v[220:227], v[70:73], v200, v201 op_sel_hi:[0,0,0]
	v_mfma_scale_f32_16x16x128_f8f6f4 v[66:69], v[10:17], v[220:227], v[66:69], v200, v201 op_sel_hi:[0,0,0]
	v_mfma_scale_f32_16x16x128_f8f6f4 v[54:57], v[2:9], v[228:235], v[54:57], v200, v201 op_sel_hi:[0,0,0]
	v_mfma_scale_f32_16x16x128_f8f6f4 v[50:53], v[10:17], v[228:235], v[50:53], v200, v201 op_sel_hi:[0,0,0]
	v_mfma_scale_f32_16x16x128_f8f6f4 v[38:41], v[2:9], v[236:243], v[38:41], v200, v201 op_sel_hi:[0,0,0]
	v_mfma_scale_f32_16x16x128_f8f6f4 v[34:37], v[10:17], v[236:243], v[34:37], v200, v201 op_sel_hi:[0,0,0]
	s_barrier
; #define PG8_STAGE(bufoff, gbase, voff) do { _Pragma("unroll") for (int _i = 0; _i < 2; ++_i) \
;         __builtin_amdgcn_global_load_lds((const unsigned*)((const char*)(gbase) + (voff)[_i]), (PG8_LAS unsigned*)(lds + (bufoff) + ldsw + _i * 8192), 16, 0, 0); } while (0)
; #define PG8_LDA(dst, b, h) do { _Pragma("unroll") for (int m = 0; m < 4; ++m) { const bf16x8 f0_ = *(const PG8_LAS bf16x8*)(lds + PG8_SA(b, h) + aoff + m * 2048), f1_ = *(const PG8_LAS bf16x8*)(lds + PG8_SA(b, h) + aoff + m * 2048 + 1024); dst[m].set(f0_, f1_); } } while (0)
; #define PG8_LDB(dst, b, h) do { _Pragma("unroll") for (int n = 0; n < 2; ++n) { const bf16x8 f0_ = *(const PG8_LAS bf16x8*)(lds + PG8_SB(b, h) + boff + n * 2048), f1_ = *(const PG8_LAS bf16x8*)(lds + PG8_SB(b, h) + boff + n * 2048 + 1024); dst[n].set(f0_, f1_); } } while (0)
; #define PG8_WAIT_V(n) asm volatile("s_waitcnt vmcnt(" #n ")" ::: "memory")
; #define PG8_WAIT_L(n) asm volatile("s_waitcnt lgkmcnt(" #n ")" ::: "memory")
; #define PG8_BAR __builtin_amdgcn_s_barrier()
; #define PG8_SCHED __builtin_amdgcn_sched_barrier(0)
; template <class Epi, class Sched, bool ALIGN_EPI = false, bool SP2 = false>
; __device__ __forceinline__ void gemm_phase(PG8_LAS unsigned char* lds, const Gemm g, const Sched& S, const Epi& E) {
;     ...
;         for (int t = 0; t < nt; t += 2) {
;             if constexpr (Epi::MIDK) { if (t == (nt >> 1)) E.mid(acc, cur, wr, wc, fr, fq); }
;             const bool last = (t == nt - 2);
;             const char* a1 = cA + (size_t)(t + 1) * kstep;
;             const char* a2 = last ? nA : cA + (size_t)(t + 2) * kstep; const char* b2 = last ? nB : cB + (size_t)(t + 2) * kstep;
;     ...
;             PG8_LDB(B0, 1, 0); PG8_LDB(B1, 1, 1); PG8_SCHED; PG8_LDA(At, 1, 0); PG8_STAGE(PG8_SA(0, 1), a2 + hstep, voffA);
;             PG8_WAIT_V(8); PG8_WAIT_L(0); PG8_BAR; PG8_MMA(0, 0, At, B0); PG8_MMA(0, 1, At, B1); PG8_BAR; PG8_SCHED;
;             PG8_LDA(At, 1, 1); PG8_STAGE(PG8_SB(1, 0), b3, voffB); PG8_STAGE(PG8_SB(1, 1), b3 + hstepB, voffB); PG8_STAGE(PG8_SA(1, 0), a3, voffA);
;             PG8_WAIT_V(8); PG8_WAIT_L(0); PG8_BAR; PG8_MMA(1, 0, At, B0); PG8_MMA(1, 1, At, B1); PG8_BAR; PG8_SCHED;
	s_setprio 0
	s_add_i32 s33, 0, 0x18000
	s_add_i32 s50, 0, 0x1c000
	v_add_u32_e32 v14, s33, v173
	v_add_u32_e32 v30, s50, v173
	ds_read_b128 v[2:5], v14
	ds_read_b128 v[6:9], v14 offset:1024
	ds_read_b128 v[10:13], v14 offset:2048
	ds_read_b128 v[14:17], v14 offset:3072
	ds_read_b128 v[18:21], v30
	ds_read_b128 v[22:25], v30 offset:1024
	ds_read_b128 v[26:29], v30 offset:2048
	ds_read_b128 v[30:33], v30 offset:3072
	s_add_u32 s0, s48, s12
	s_addc_u32 s1, s49, s13
	s_mov_b32 m0, s52
	v_lshl_add_u64 v[204:205], s[0:1], 0, v[162:163]
	ds_read_b128 v[212:215], v199 offset:32768
	ds_read_b128 v[216:219], v199 offset:33792
	ds_read_b128 v[220:223], v199 offset:34816
	ds_read_b128 v[224:227], v199 offset:35840
	ds_read_b128 v[228:231], v199 offset:36864
	ds_read_b128 v[232:235], v199 offset:37888
	ds_read_b128 v[236:239], v199 offset:38912
	ds_read_b128 v[240:243], v199 offset:39936
	s_mov_b32 m0, s10
	s_nop 0
	global_load_lds_dwordx4 v[192:193], off
	s_mov_b32 m0, s11
	s_nop 0
	global_load_lds_dwordx4 v[194:195], off
	s_mov_b32 m0, s52
	s_nop 0
	global_load_lds_dwordx4 v[204:205], off
	v_lshl_add_u64 v[204:205], s[0:1], 0, v[166:167]
	s_mov_b32 m0, s53
	s_nop 0
	global_load_lds_dwordx4 v[204:205], off
	s_waitcnt vmcnt(8)
	s_waitcnt lgkmcnt(0)
	s_barrier
	s_setprio 1
	s_waitcnt lgkmcnt(0)
	v_mfma_scale_f32_16x16x128_f8f6f4 v[158:161], v[2:9], v[212:219], v[158:161], v200, v201 op_sel_hi:[0,0,0]
	v_mfma_scale_f32_16x16x128_f8f6f4 v[154:157], v[10:17], v[212:219], v[154:157], v200, v201 op_sel_hi:[0,0,0]
	v_mfma_scale_f32_16x16x128_f8f6f4 v[142:145], v[2:9], v[220:227], v[142:145], v200, v201 op_sel_hi:[0,0,0]
	v_mfma_scale_f32_16x16x128_f8f6f4 v[138:141], v[10:17], v[220:227], v[138:141], v200, v201 op_sel_hi:[0,0,0]
	v_mfma_scale_f32_16x16x128_f8f6f4 v[126:129], v[2:9], v[228:235], v[126:129], v200, v201 op_sel_hi:[0,0,0]
	v_mfma_scale_f32_16x16x128_f8f6f4 v[122:125], v[10:17], v[228:235], v[122:125], v200, v201 op_sel_hi:[0,0,0]
	v_mfma_scale_f32_16x16x128_f8f6f4 v[110:113], v[2:9], v[236:243], v[110:113], v200, v201 op_sel_hi:[0,0,0]
	v_mfma_scale_f32_16x16x128_f8f6f4 v[106:109], v[10:17], v[236:243], v[106:109], v200, v201 op_sel_hi:[0,0,0]
	v_mfma_scale_f32_16x16x128_f8f6f4 v[150:153], v[18:25], v[212:219], v[150:153], v200, v201 op_sel_hi:[0,0,0]
	v_mfma_scale_f32_16x16x128_f8f6f4 v[146:149], v[26:33], v[212:219], v[146:149], v200, v201 op_sel_hi:[0,0,0]
	v_mfma_scale_f32_16x16x128_f8f6f4 v[134:137], v[18:25], v[220:227], v[134:137], v200, v201 op_sel_hi:[0,0,0]
	v_mfma_scale_f32_16x16x128_f8f6f4 v[130:133], v[26:33], v[220:227], v[130:133], v200, v201 op_sel_hi:[0,0,0]
	v_mfma_scale_f32_16x16x128_f8f6f4 v[118:121], v[18:25], v[228:235], v[118:121], v200, v201 op_sel_hi:[0,0,0]
	v_mfma_scale_f32_16x16x128_f8f6f4 v[114:117], v[26:33], v[228:235], v[114:117], v200, v201 op_sel_hi:[0,0,0]
	v_mfma_scale_f32_16x16x128_f8f6f4 v[102:105], v[18:25], v[236:243], v[102:105], v200, v201 op_sel_hi:[0,0,0]
	v_mfma_scale_f32_16x16x128_f8f6f4 v[98:101], v[26:33], v[236:243], v[98:101], v200, v201 op_sel_hi:[0,0,0]
	s_barrier
	s_setprio 0
	s_add_i32 s0, s33, s9
	v_lshl_add_u64 v[184:185], v[184:185], 0, s[28:29]
	s_mov_b32 m0, s0
	ds_read_b128 v[212:215], v199 offset:49152
	ds_read_b128 v[216:219], v199 offset:50176
	ds_read_b128 v[220:223], v199 offset:51200
	ds_read_b128 v[224:227], v199 offset:52224
	ds_read_b128 v[228:231], v199 offset:53248
	ds_read_b128 v[232:235], v199 offset:54272
	ds_read_b128 v[236:239], v199 offset:55296
	ds_read_b128 v[240:243], v199 offset:56320
	global_load_lds_dwordx4 v[184:185], off
	v_lshl_add_u64 v[184:185], v[186:187], 0, s[28:29]
	s_add_i32 m0, s0, 0x2000
	s_add_i32 s0, s50, s9
	global_load_lds_dwordx4 v[184:185], off
	v_lshl_add_u64 v[184:185], v[188:189], 0, s[28:29]
	s_mov_b32 m0, s0
	s_nop 0
	global_load_lds_dwordx4 v[184:185], off
	v_lshl_add_u64 v[184:185], v[190:191], 0, s[28:29]
	s_add_i32 m0, s0, 0x2000
	s_nop 0
	global_load_lds_dwordx4 v[184:185], off
	s_cmp_ge_i32 s82, s58
	s_cbranch_scc0 .Lkr5_b
	v_lshl_add_u64 v[184:185], v[192:193], 0, s[28:29]
	s_mov_b32 m0, s56
	s_nop 0
	global_load_lds_dwordx4 v[184:185], off
	v_lshl_add_u64 v[184:185], v[194:195], 0, s[28:29]
	s_mov_b32 m0, s57
	s_nop 0
	global_load_lds_dwordx4 v[184:185], off
.Lkr5_b:
	s_waitcnt vmcnt(6)
	s_waitcnt lgkmcnt(0)
	s_barrier
	s_setprio 1
	s_waitcnt lgkmcnt(0)
	v_mfma_scale_f32_16x16x128_f8f6f4 v[94:97], v[2:9], v[212:219], v[94:97], v200, v201 op_sel_hi:[0,0,0]
	v_mfma_scale_f32_16x16x128_f8f6f4 v[90:93], v[10:17], v[212:219], v[90:93], v200, v201 op_sel_hi:[0,0,0]
	v_mfma_scale_f32_16x16x128_f8f6f4 v[78:81], v[2:9], v[220:227], v[78:81], v200, v201 op_sel_hi:[0,0,0]
	v_mfma_scale_f32_16x16x128_f8f6f4 v[74:77], v[10:17], v[220:227], v[74:77], v200, v201 op_sel_hi:[0,0,0]
	v_mfma_scale_f32_16x16x128_f8f6f4 v[62:65], v[2:9], v[228:235], v[62:65], v200, v201 op_sel_hi:[0,0,0]
	v_mfma_scale_f32_16x16x128_f8f6f4 v[58:61], v[10:17], v[228:235], v[58:61], v200, v201 op_sel_hi:[0,0,0]
	v_mfma_scale_f32_16x16x128_f8f6f4 v[46:49], v[2:9], v[236:243], v[46:49], v200, v201 op_sel_hi:[0,0,0]
	v_mfma_scale_f32_16x16x128_f8f6f4 v[42:45], v[10:17], v[236:243], v[42:45], v200, v201 op_sel_hi:[0,0,0]
	v_mfma_scale_f32_16x16x128_f8f6f4 v[86:89], v[18:25], v[212:219], v[86:89], v200, v201 op_sel_hi:[0,0,0]
	v_mfma_scale_f32_16x16x128_f8f6f4 v[82:85], v[26:33], v[212:219], v[82:85], v200, v201 op_sel_hi:[0,0,0]
	v_mfma_scale_f32_16x16x128_f8f6f4 v[70:73], v[18:25], v[220:227], v[70:73], v200, v201 op_sel_hi:[0,0,0]
	v_mfma_scale_f32_16x16x128_f8f6f4 v[66:69], v[26:33], v[220:227], v[66:69], v200, v201 op_sel_hi:[0,0,0]
	v_mfma_scale_f32_16x16x128_f8f6f4 v[54:57], v[18:25], v[228:235], v[54:57], v200, v201 op_sel_hi:[0,0,0]
	v_mfma_scale_f32_16x16x128_f8f6f4 v[50:53], v[26:33], v[228:235], v[50:53], v200, v201 op_sel_hi:[0,0,0]
	v_mfma_scale_f32_16x16x128_f8f6f4 v[38:41], v[18:25], v[236:243], v[38:41], v200, v201 op_sel_hi:[0,0,0]
	v_mfma_scale_f32_16x16x128_f8f6f4 v[34:37], v[26:33], v[236:243], v[34:37], v200, v201 op_sel_hi:[0,0,0]
	s_barrier
	s_setprio 0
	s_add_u32 s46, s46, 0x100
	s_addc_u32 s47, s47, 0
	s_add_u32 s80, s80, 0x100
	s_addc_u32 s81, s81, 0
	s_cmp_ge_i32 s82, s58
	s_cselect_b32 s99, 0, 1
	s_mov_b32 s48, s82
	s_cbranch_scc0 .LBB0_1625

; #define PG8_STAGE(bufoff, gbase, voff) do { _Pragma("unroll") for (int _i = 0; _i < 2; ++_i) \
;         __builtin_amdgcn_global_load_lds((const unsigned*)((const char*)(gbase) + (voff)[_i]), (PG8_LAS unsigned*)(lds + (bufoff) + ldsw + _i * 8192), 16, 0, 0); } while (0)
; #define PG8_LDA(dst, b, h) do { _Pragma("unroll") for (int m = 0; m < 4; ++m) { const bf16x8 f0_ = *(const PG8_LAS bf16x8*)(lds + PG8_SA(b, h) + aoff + m * 2048), f1_ = *(const PG8_LAS bf16x8*)(lds + PG8_SA(b, h) + aoff + m * 2048 + 1024); dst[m].set(f0_, f1_); } } while (0)
; #define PG8_LDB(dst, b, h) do { _Pragma("unroll") for (int n = 0; n < 2; ++n) { const bf16x8 f0_ = *(const PG8_LAS bf16x8*)(lds + PG8_SB(b, h) + boff + n * 2048), f1_ = *(const PG8_LAS bf16x8*)(lds + PG8_SB(b, h) + boff + n * 2048 + 1024); dst[n].set(f0_, f1_); } } while (0)
; #define PG8_WAIT_V(n) asm volatile("s_waitcnt vmcnt(" #n ")" ::: "memory")
; #define PG8_WAIT_L(n) asm volatile("s_waitcnt lgkmcnt(" #n ")" ::: "memory")
; #define PG8_BAR __builtin_amdgcn_s_barrier()
; #define PG8_SCHED __builtin_amdgcn_sched_barrier(0)
; template <class Epi, class Sched, bool ALIGN_EPI = false, bool SP2 = false>
; __device__ __forceinline__ void gemm_phase(PG8_LAS unsigned char* lds, const Gemm g, const Sched& S, const Epi& E) {
;     ...
;             PG8_LDB(B0, 0, 0); PG8_LDB(B1, 0, 1); PG8_SCHED; PG8_LDA(At, 0, 0); PG8_STAGE(PG8_SA(1, 1), a1 + hstep, voffA);
;             PG8_WAIT_V(8); PG8_WAIT_L(0); PG8_BAR; PG8_MMA(0, 0, At, B0); PG8_MMA(0, 1, At, B1); PG8_BAR; PG8_SCHED;
;             PG8_LDA(At, 0, 1); PG8_STAGE(PG8_SB(0, 0), b2, voffB); PG8_STAGE(PG8_SB(0, 1), b2 + hstepB, voffB); PG8_STAGE(PG8_SA(0, 0), a2, voffA);
;             PG8_WAIT_V(8); PG8_WAIT_L(0); PG8_BAR; PG8_MMA(1, 0, At, B0); PG8_MMA(1, 1, At, B1); PG8_BAR; PG8_SCHED;
.Lkr6_a:
	v_lshl_add_u64 v[206:207], s[2:3], 0, v[198:199]
	s_add_i32 m0, s71, 0xc000
	ds_read_b128 v[152:155], v217
	ds_read_b128 v[156:159], v217 offset:1024
	ds_read_b128 v[168:171], v217 offset:2048
	ds_read_b128 v[172:175], v217 offset:3072
	ds_read_b128 v[176:179], v217 offset:4096
	ds_read_b128 v[180:183], v217 offset:5120
	ds_read_b128 v[226:229], v217 offset:6144
	ds_read_b128 v[230:233], v217 offset:7168
	global_load_lds_dwordx4 v[206:207], off
	v_lshl_add_u64 v[206:207], s[2:3], 0, v[200:201]
	s_add_i32 m0, s71, 0xe000
	s_nop 0
	global_load_lds_dwordx4 v[206:207], off
	s_waitcnt vmcnt(8)
	s_waitcnt lgkmcnt(0)
	s_barrier
	s_setprio 1
	s_waitcnt lgkmcnt(0)
	v_mfma_scale_f32_16x16x128_f8f6f4 v[164:167], v[16:23], v[152:159], v[164:167], v218, v219 op_sel_hi:[0,0,0]
	v_mfma_scale_f32_16x16x128_f8f6f4 v[160:163], v[24:31], v[152:159], v[160:163], v218, v219 op_sel_hi:[0,0,0]
	v_mfma_scale_f32_16x16x128_f8f6f4 v[140:143], v[16:23], v[168:175], v[140:143], v218, v219 op_sel_hi:[0,0,0]
	v_mfma_scale_f32_16x16x128_f8f6f4 v[136:139], v[24:31], v[168:175], v[136:139], v218, v219 op_sel_hi:[0,0,0]
	v_mfma_scale_f32_16x16x128_f8f6f4 v[108:111], v[16:23], v[176:183], v[108:111], v218, v219 op_sel_hi:[0,0,0]
	v_mfma_scale_f32_16x16x128_f8f6f4 v[104:107], v[24:31], v[176:183], v[104:107], v218, v219 op_sel_hi:[0,0,0]
	v_mfma_scale_f32_16x16x128_f8f6f4 v[116:119], v[16:23], v[226:233], v[116:119], v218, v219 op_sel_hi:[0,0,0]
	v_mfma_scale_f32_16x16x128_f8f6f4 v[112:115], v[24:31], v[226:233], v[112:115], v218, v219 op_sel_hi:[0,0,0]
	v_mfma_scale_f32_16x16x128_f8f6f4 v[148:151], v[0:7], v[152:159], v[148:151], v218, v219 op_sel_hi:[0,0,0]
	v_mfma_scale_f32_16x16x128_f8f6f4 v[144:147], v[8:15], v[152:159], v[144:147], v218, v219 op_sel_hi:[0,0,0]
	v_mfma_scale_f32_16x16x128_f8f6f4 v[132:135], v[0:7], v[168:175], v[132:135], v218, v219 op_sel_hi:[0,0,0]
	v_mfma_scale_f32_16x16x128_f8f6f4 v[128:131], v[8:15], v[168:175], v[128:131], v218, v219 op_sel_hi:[0,0,0]
	v_mfma_scale_f32_16x16x128_f8f6f4 v[124:127], v[0:7], v[176:183], v[124:127], v218, v219 op_sel_hi:[0,0,0]
	v_mfma_scale_f32_16x16x128_f8f6f4 v[120:123], v[8:15], v[176:183], v[120:123], v218, v219 op_sel_hi:[0,0,0]
	v_mfma_scale_f32_16x16x128_f8f6f4 v[100:103], v[0:7], v[226:233], v[100:103], v218, v219 op_sel_hi:[0,0,0]
	v_mfma_scale_f32_16x16x128_f8f6f4 v[96:99], v[8:15], v[226:233], v[96:99], v218, v219 op_sel_hi:[0,0,0]
	s_barrier
	s_setprio 0
	s_add_i32 s0, s67, s45
	v_lshl_add_u64 v[152:153], s[80:81], 0, v[186:187]
	s_mov_b32 m0, s0
	ds_read_b128 v[172:175], v217 offset:16384
	ds_read_b128 v[176:179], v217 offset:17408
	ds_read_b128 v[226:229], v217 offset:18432
	ds_read_b128 v[230:233], v217 offset:19456
	ds_read_b128 v[234:237], v217 offset:20480
	ds_read_b128 v[238:241], v217 offset:21504
	ds_read_b128 v[242:245], v217 offset:22528
	ds_read_b128 v[246:249], v217 offset:23552
	global_load_lds_dwordx4 v[152:153], off
	s_add_i32 m0, s0, 0x2000
	s_add_u32 s0, s80, s20
	v_lshl_add_u64 v[154:155], s[80:81], 0, v[190:191]
	s_addc_u32 s1, s81, s21
	s_add_i32 s33, s10, s45
	global_load_lds_dwordx4 v[154:155], off
	v_lshl_add_u64 v[156:157], s[0:1], 0, v[186:187]
	s_mov_b32 m0, s33
	v_lshl_add_u64 v[158:159], s[0:1], 0, v[190:191]
	global_load_lds_dwordx4 v[156:157], off
	s_add_i32 m0, s33, 0x2000
	v_lshl_add_u64 v[168:169], s[78:79], 0, v[184:185]
	global_load_lds_dwordx4 v[158:159], off
	v_lshl_add_u64 v[170:171], s[78:79], 0, v[188:189]
	s_waitcnt vmcnt(6)
	s_waitcnt lgkmcnt(0)
	s_barrier
	s_setprio 1
	s_waitcnt lgkmcnt(0)
	v_mfma_scale_f32_16x16x128_f8f6f4 v[92:95], v[16:23], v[172:179], v[92:95], v218, v219 op_sel_hi:[0,0,0]
	v_mfma_scale_f32_16x16x128_f8f6f4 v[88:91], v[24:31], v[172:179], v[88:91], v218, v219 op_sel_hi:[0,0,0]
	v_mfma_scale_f32_16x16x128_f8f6f4 v[76:79], v[16:23], v[226:233], v[76:79], v218, v219 op_sel_hi:[0,0,0]
	v_mfma_scale_f32_16x16x128_f8f6f4 v[72:75], v[24:31], v[226:233], v[72:75], v218, v219 op_sel_hi:[0,0,0]
	v_mfma_scale_f32_16x16x128_f8f6f4 v[60:63], v[16:23], v[234:241], v[60:63], v218, v219 op_sel_hi:[0,0,0]
	v_mfma_scale_f32_16x16x128_f8f6f4 v[56:59], v[24:31], v[234:241], v[56:59], v218, v219 op_sel_hi:[0,0,0]
	v_mfma_scale_f32_16x16x128_f8f6f4 v[44:47], v[16:23], v[242:249], v[44:47], v218, v219 op_sel_hi:[0,0,0]
	v_mfma_scale_f32_16x16x128_f8f6f4 v[40:43], v[24:31], v[242:249], v[40:43], v218, v219 op_sel_hi:[0,0,0]
	v_mfma_scale_f32_16x16x128_f8f6f4 v[84:87], v[0:7], v[172:179], v[84:87], v218, v219 op_sel_hi:[0,0,0]
	v_mfma_scale_f32_16x16x128_f8f6f4 v[80:83], v[8:15], v[172:179], v[80:83], v218, v219 op_sel_hi:[0,0,0]
	v_mfma_scale_f32_16x16x128_f8f6f4 v[68:71], v[0:7], v[226:233], v[68:71], v218, v219 op_sel_hi:[0,0,0]
	v_mfma_scale_f32_16x16x128_f8f6f4 v[64:67], v[8:15], v[226:233], v[64:67], v218, v219 op_sel_hi:[0,0,0]
	v_mfma_scale_f32_16x16x128_f8f6f4 v[52:55], v[0:7], v[234:241], v[52:55], v218, v219 op_sel_hi:[0,0,0]
	v_mfma_scale_f32_16x16x128_f8f6f4 v[48:51], v[8:15], v[234:241], v[48:51], v218, v219 op_sel_hi:[0,0,0]
	v_mfma_scale_f32_16x16x128_f8f6f4 v[36:39], v[0:7], v[242:249], v[36:39], v218, v219 op_sel_hi:[0,0,0]
	v_mfma_scale_f32_16x16x128_f8f6f4 v[32:35], v[8:15], v[242:249], v[32:35], v218, v219 op_sel_hi:[0,0,0]
	s_barrier
; #define PG8_STAGE(bufoff, gbase, voff) do { _Pragma("unroll") for (int _i = 0; _i < 2; ++_i) \
;         __builtin_amdgcn_global_load_lds((const unsigned*)((const char*)(gbase) + (voff)[_i]), (PG8_LAS unsigned*)(lds + (bufoff) + ldsw + _i * 8192), 16, 0, 0); } while (0)
; #define PG8_LDA(dst, b, h) do { _Pragma("unroll") for (int m = 0; m < 4; ++m) { const bf16x8 f0_ = *(const PG8_LAS bf16x8*)(lds + PG8_SA(b, h) + aoff + m * 2048), f1_ = *(const PG8_LAS bf16x8*)(lds + PG8_SA(b, h) + aoff + m * 2048 + 1024); dst[m].set(f0_, f1_); } } while (0)
; #define PG8_LDB(dst, b, h) do { _Pragma("unroll") for (int n = 0; n < 2; ++n) { const bf16x8 f0_ = *(const PG8_LAS bf16x8*)(lds + PG8_SB(b, h) + boff + n * 2048), f1_ = *(const PG8_LAS bf16x8*)(lds + PG8_SB(b, h) + boff + n * 2048 + 1024); dst[n].set(f0_, f1_); } } while (0)
; #define PG8_WAIT_V(n) asm volatile("s_waitcnt vmcnt(" #n ")" ::: "memory")
; #define PG8_WAIT_L(n) asm volatile("s_waitcnt lgkmcnt(" #n ")" ::: "memory")
; #define PG8_BAR __builtin_amdgcn_s_barrier()
; #define PG8_SCHED __builtin_amdgcn_sched_barrier(0)
; template <class Epi, class Sched, bool ALIGN_EPI = false, bool SP2 = false>
; __device__ __forceinline__ void gemm_phase(PG8_LAS unsigned char* lds, const Gemm g, const Sched& S, const Epi& E) {
;     ...
;         for (int t = 0; t < nt; t += 2) {
;             if constexpr (Epi::MIDK) { if (t == (nt >> 1)) E.mid(acc, cur, wr, wc, fr, fq); }
;             const bool last = (t == nt - 2);
;             const char* a1 = cA + (size_t)(t + 1) * kstep;
;             const char* a2 = last ? nA : cA + (size_t)(t + 2) * kstep; const char* b2 = last ? nB : cB + (size_t)(t + 2) * kstep;
;     ...
;             PG8_LDB(B0, 1, 0); PG8_LDB(B1, 1, 1); PG8_SCHED; PG8_LDA(At, 1, 0); PG8_STAGE(PG8_SA(0, 1), a2 + hstep, voffA);
;             PG8_WAIT_V(8); PG8_WAIT_L(0); PG8_BAR; PG8_MMA(0, 0, At, B0); PG8_MMA(0, 1, At, B1); PG8_BAR; PG8_SCHED;
;             PG8_LDA(At, 1, 1); PG8_STAGE(PG8_SB(1, 0), b3, voffB); PG8_STAGE(PG8_SB(1, 1), b3 + hstepB, voffB); PG8_STAGE(PG8_SA(1, 0), a3, voffA);
;             PG8_WAIT_V(8); PG8_WAIT_L(0); PG8_BAR; PG8_MMA(1, 0, At, B0); PG8_MMA(1, 1, At, B1); PG8_BAR; PG8_SCHED;
	s_setprio 0
	s_add_i32 s33, 0, 0x18000
	s_add_i32 s80, 0, 0x1c000
	v_add_u32_e32 v12, s33, v211
	v_add_u32_e32 v28, s80, v211
	ds_read_b128 v[0:3], v12
	ds_read_b128 v[4:7], v12 offset:1024
	ds_read_b128 v[8:11], v12 offset:2048
	ds_read_b128 v[12:15], v12 offset:3072
	ds_read_b128 v[16:19], v28
	ds_read_b128 v[20:23], v28 offset:1024
	ds_read_b128 v[24:27], v28 offset:2048
	ds_read_b128 v[28:31], v28 offset:3072
	s_add_u32 s0, s78, s18
	s_addc_u32 s1, s79, s19
	s_mov_b32 m0, s86
	v_lshl_add_u64 v[180:181], s[0:1], 0, v[184:185]
	ds_read_b128 v[172:175], v217 offset:32768
	ds_read_b128 v[176:179], v217 offset:33792
	ds_read_b128 v[226:229], v217 offset:34816
	ds_read_b128 v[230:233], v217 offset:35840
	ds_read_b128 v[234:237], v217 offset:36864
	ds_read_b128 v[238:241], v217 offset:37888
	ds_read_b128 v[242:245], v217 offset:38912
	ds_read_b128 v[246:249], v217 offset:39936
	s_mov_b32 m0, s71
	s_nop 0
	global_load_lds_dwordx4 v[168:169], off
	s_mov_b32 m0, s73
	s_nop 0
	global_load_lds_dwordx4 v[170:171], off
	s_mov_b32 m0, s86
	s_nop 0
	global_load_lds_dwordx4 v[180:181], off
	v_lshl_add_u64 v[180:181], s[0:1], 0, v[188:189]
	s_mov_b32 m0, s87
	s_nop 0
	global_load_lds_dwordx4 v[180:181], off
	s_waitcnt vmcnt(8)
	s_waitcnt lgkmcnt(0)
	s_barrier
	s_setprio 1
	s_waitcnt lgkmcnt(0)
	v_mfma_scale_f32_16x16x128_f8f6f4 v[164:167], v[0:7], v[172:179], v[164:167], v218, v219 op_sel_hi:[0,0,0]
	v_mfma_scale_f32_16x16x128_f8f6f4 v[160:163], v[8:15], v[172:179], v[160:163], v218, v219 op_sel_hi:[0,0,0]
	v_mfma_scale_f32_16x16x128_f8f6f4 v[140:143], v[0:7], v[226:233], v[140:143], v218, v219 op_sel_hi:[0,0,0]
	v_mfma_scale_f32_16x16x128_f8f6f4 v[136:139], v[8:15], v[226:233], v[136:139], v218, v219 op_sel_hi:[0,0,0]
	v_mfma_scale_f32_16x16x128_f8f6f4 v[108:111], v[0:7], v[234:241], v[108:111], v218, v219 op_sel_hi:[0,0,0]
	v_mfma_scale_f32_16x16x128_f8f6f4 v[104:107], v[8:15], v[234:241], v[104:107], v218, v219 op_sel_hi:[0,0,0]
	v_mfma_scale_f32_16x16x128_f8f6f4 v[116:119], v[0:7], v[242:249], v[116:119], v218, v219 op_sel_hi:[0,0,0]
	v_mfma_scale_f32_16x16x128_f8f6f4 v[112:115], v[8:15], v[242:249], v[112:115], v218, v219 op_sel_hi:[0,0,0]
	v_mfma_scale_f32_16x16x128_f8f6f4 v[148:151], v[16:23], v[172:179], v[148:151], v218, v219 op_sel_hi:[0,0,0]
	v_mfma_scale_f32_16x16x128_f8f6f4 v[144:147], v[24:31], v[172:179], v[144:147], v218, v219 op_sel_hi:[0,0,0]
	v_mfma_scale_f32_16x16x128_f8f6f4 v[132:135], v[16:23], v[226:233], v[132:135], v218, v219 op_sel_hi:[0,0,0]
	v_mfma_scale_f32_16x16x128_f8f6f4 v[128:131], v[24:31], v[226:233], v[128:131], v218, v219 op_sel_hi:[0,0,0]
	v_mfma_scale_f32_16x16x128_f8f6f4 v[124:127], v[16:23], v[234:241], v[124:127], v218, v219 op_sel_hi:[0,0,0]
	v_mfma_scale_f32_16x16x128_f8f6f4 v[120:123], v[24:31], v[234:241], v[120:123], v218, v219 op_sel_hi:[0,0,0]
	v_mfma_scale_f32_16x16x128_f8f6f4 v[100:103], v[16:23], v[242:249], v[100:103], v218, v219 op_sel_hi:[0,0,0]
	v_mfma_scale_f32_16x16x128_f8f6f4 v[96:99], v[24:31], v[242:249], v[96:99], v218, v219 op_sel_hi:[0,0,0]
	s_barrier
	s_setprio 0
	s_add_i32 s0, s33, s45
	v_lshl_add_u64 v[152:153], v[152:153], 0, s[36:37]
	s_mov_b32 m0, s0
	ds_read_b128 v[172:175], v217 offset:49152
	ds_read_b128 v[176:179], v217 offset:50176
	ds_read_b128 v[226:229], v217 offset:51200
	ds_read_b128 v[230:233], v217 offset:52224
	ds_read_b128 v[234:237], v217 offset:53248
	ds_read_b128 v[238:241], v217 offset:54272
	ds_read_b128 v[242:245], v217 offset:55296
	ds_read_b128 v[246:249], v217 offset:56320
	global_load_lds_dwordx4 v[152:153], off
	v_lshl_add_u64 v[152:153], v[154:155], 0, s[36:37]
	s_add_i32 m0, s0, 0x2000
	s_add_i32 s0, s80, s45
	global_load_lds_dwordx4 v[152:153], off
	v_lshl_add_u64 v[152:153], v[156:157], 0, s[36:37]
	s_mov_b32 m0, s0
	s_nop 0
	global_load_lds_dwordx4 v[152:153], off
	v_lshl_add_u64 v[152:153], v[158:159], 0, s[36:37]
	s_add_i32 m0, s0, 0x2000
	s_nop 0
	global_load_lds_dwordx4 v[152:153], off
	s_cmp_ge_i32 s83, s91
	s_cbranch_scc0 .Lkr6_b
	v_lshl_add_u64 v[152:153], v[168:169], 0, s[36:37]
	s_mov_b32 m0, s93
	s_nop 0
	global_load_lds_dwordx4 v[152:153], off
	v_lshl_add_u64 v[152:153], v[170:171], 0, s[36:37]
	s_mov_b32 m0, s94
	s_nop 0
	global_load_lds_dwordx4 v[152:153], off
.Lkr6_b:
	s_waitcnt vmcnt(6)
	s_waitcnt lgkmcnt(0)
	s_barrier
	s_setprio 1
	s_waitcnt lgkmcnt(0)
	v_mfma_scale_f32_16x16x128_f8f6f4 v[92:95], v[0:7], v[172:179], v[92:95], v218, v219 op_sel_hi:[0,0,0]
	v_mfma_scale_f32_16x16x128_f8f6f4 v[88:91], v[8:15], v[172:179], v[88:91], v218, v219 op_sel_hi:[0,0,0]
	v_mfma_scale_f32_16x16x128_f8f6f4 v[76:79], v[0:7], v[226:233], v[76:79], v218, v219 op_sel_hi:[0,0,0]
	v_mfma_scale_f32_16x16x128_f8f6f4 v[72:75], v[8:15], v[226:233], v[72:75], v218, v219 op_sel_hi:[0,0,0]
	v_mfma_scale_f32_16x16x128_f8f6f4 v[60:63], v[0:7], v[234:241], v[60:63], v218, v219 op_sel_hi:[0,0,0]
	v_mfma_scale_f32_16x16x128_f8f6f4 v[56:59], v[8:15], v[234:241], v[56:59], v218, v219 op_sel_hi:[0,0,0]
	v_mfma_scale_f32_16x16x128_f8f6f4 v[44:47], v[0:7], v[242:249], v[44:47], v218, v219 op_sel_hi:[0,0,0]
	v_mfma_scale_f32_16x16x128_f8f6f4 v[40:43], v[8:15], v[242:249], v[40:43], v218, v219 op_sel_hi:[0,0,0]
	v_mfma_scale_f32_16x16x128_f8f6f4 v[84:87], v[16:23], v[172:179], v[84:87], v218, v219 op_sel_hi:[0,0,0]
	v_mfma_scale_f32_16x16x128_f8f6f4 v[80:83], v[24:31], v[172:179], v[80:83], v218, v219 op_sel_hi:[0,0,0]
	v_mfma_scale_f32_16x16x128_f8f6f4 v[68:71], v[16:23], v[226:233], v[68:71], v218, v219 op_sel_hi:[0,0,0]
	v_mfma_scale_f32_16x16x128_f8f6f4 v[64:67], v[24:31], v[226:233], v[64:67], v218, v219 op_sel_hi:[0,0,0]
	v_mfma_scale_f32_16x16x128_f8f6f4 v[52:55], v[16:23], v[234:241], v[52:55], v218, v219 op_sel_hi:[0,0,0]
	v_mfma_scale_f32_16x16x128_f8f6f4 v[48:51], v[24:31], v[234:241], v[48:51], v218, v219 op_sel_hi:[0,0,0]
	v_mfma_scale_f32_16x16x128_f8f6f4 v[36:39], v[16:23], v[242:249], v[36:39], v218, v219 op_sel_hi:[0,0,0]
	v_mfma_scale_f32_16x16x128_f8f6f4 v[32:35], v[24:31], v[242:249], v[32:35], v218, v219 op_sel_hi:[0,0,0]
	s_barrier
	s_setprio 0
	s_add_u32 s2, s2, 0x100
	s_addc_u32 s3, s3, 0
	s_add_u32 s57, s57, 0x100
	s_addc_u32 s82, s82, 0
	s_cmp_ge_i32 s83, s91
	s_cselect_b32 s99, 0, 1
	s_mov_b32 s78, s83
	s_cbranch_scc0 .LBB0_1658
